# accumulate chains (k=0,1 back to back) in the five GEMM steady loops + static s_setprio 1 for waves 0-3, flips deleted + compiler vmcnt(0) dropped
# speedup vs baseline: 1.0137x; 1.0049x over previous
;     __device__ bool next(int i, Unit& u) const { const int rounds = nwg / G; if (i >= rounds) return false; return StaticOrder::next(rounds - 1 - i, u); }
;     __device__ bool next(int i, Unit& u) const { const int rounds = nwg / G; if (i >= 2 * rounds) return false; const bool ok = StaticOrder::next(i >= rounds ? i - rounds : i, u); u.z = (i >= rounds) ? 1 : 0; return ok; }
; template <class Epi, class Sched, bool ALIGN_EPI = false, bool SP2 = false>
; __device__ __forceinline__ void gemm_phase(PG8_LAS unsigned char* lds, const Gemm g, const Sched& S, const Epi& E) {
;     ...
;         const bool has_next = S.next(ui + 1, nxt);
;         const char* nA = has_next ? (const char*)S.opA(g, nxt) + (size_t)nxt.pm * tstepA : cA; const char* nB = has_next ? (const char*)S.opB(g, nxt) + (size_t)nxt.pn * tstepB : cB;
.LBB0_129:
	s_ashr_i32 s23, s22, 31
	s_lshl_b64 s[4:5], s[22:23], 20
	s_add_u32 s26, s34, s4
	s_addc_u32 s27, s35, s5
	s_add_i32 s45, 0, 0x10000
	s_add_i32 s47, 0, 0x14000
	v_add_u32_e32 v140, s45, v160
	v_add_u32_e32 v141, s47, v160
	ds_read_b128 v[4:7], v140
	ds_read_b128 v[8:11], v140 offset:1024
	ds_read_b128 v[12:15], v140 offset:2048
	ds_read_b128 v[16:19], v140 offset:3072
	ds_read_b128 v[20:23], v141
	ds_read_b128 v[24:27], v141 offset:1024
	ds_read_b128 v[28:31], v141 offset:2048
	ds_read_b128 v[32:35], v141 offset:3072
	s_and_b64 s[4:5], s[10:11], exec
	s_cselect_b32 s4, s27, s29
	s_cselect_b32 s5, s26, s28
	v_lshl_add_u64 v[184:185], s[30:31], 0, v[134:135]
	s_mov_b64 s[10:11], 0x84080
	s_add_i32 s23, s37, 0xc000
	v_lshl_add_u64 v[68:69], v[184:185], 0, s[10:11]
	s_mov_b32 m0, s23
	s_mov_b64 s[10:11], 0xc6080
	s_add_i32 s33, s37, 0xe000
	ds_read_b128 v[36:39], v163
	ds_read_b128 v[40:43], v163 offset:1024
	ds_read_b128 v[44:47], v163 offset:2048
	ds_read_b128 v[48:51], v163 offset:3072
	ds_read_b128 v[52:55], v163 offset:4096
	ds_read_b128 v[56:59], v163 offset:5120
	ds_read_b128 v[60:63], v163 offset:6144
	ds_read_b128 v[64:67], v163 offset:7168
	global_load_lds_dwordx4 v[68:69], off
	v_lshl_add_u64 v[68:69], v[184:185], 0, s[10:11]
	s_mov_b32 m0, s33
	s_nop 0
	global_load_lds_dwordx4 v[68:69], off
	s_waitcnt vmcnt(16)
	s_waitcnt lgkmcnt(0)
	s_barrier
	s_waitcnt lgkmcnt(0)
	v_mfma_f32_16x16x32_bf16 v[88:91], v[12:15], v[52:55], 0
	v_mfma_f32_16x16x32_bf16 v[92:95], v[16:19], v[56:59], v[88:91]
	v_mfma_f32_16x16x32_bf16 v[88:91], v[4:7], v[60:63], 0
	v_mfma_f32_16x16x32_bf16 v[68:71], v[4:7], v[36:39], 0
	v_mfma_f32_16x16x32_bf16 v[72:75], v[12:15], v[36:39], 0
	v_mfma_f32_16x16x32_bf16 v[76:79], v[4:7], v[44:47], 0
	v_mfma_f32_16x16x32_bf16 v[80:83], v[12:15], v[44:47], 0
	v_mfma_f32_16x16x32_bf16 v[84:87], v[4:7], v[52:55], 0
	v_mfma_f32_16x16x32_bf16 v[96:99], v[8:11], v[64:67], v[88:91]
	v_mfma_f32_16x16x32_bf16 v[88:91], v[12:15], v[60:63], 0
	v_mfma_f32_16x16x32_bf16 v[68:71], v[8:11], v[40:43], v[68:71]
	v_mfma_f32_16x16x32_bf16 v[72:75], v[16:19], v[40:43], v[72:75]
	v_mfma_f32_16x16x32_bf16 v[76:79], v[8:11], v[48:51], v[76:79]
	v_mfma_f32_16x16x32_bf16 v[80:83], v[16:19], v[48:51], v[80:83]
	v_mfma_f32_16x16x32_bf16 v[84:87], v[8:11], v[56:59], v[84:87]
	v_mfma_f32_16x16x32_bf16 v[108:111], v[16:19], v[64:67], v[88:91]
	v_mfma_f32_16x16x32_bf16 v[88:91], v[20:23], v[36:39], 0
	v_mfma_f32_16x16x32_bf16 v[36:39], v[28:31], v[36:39], 0
	v_mfma_f32_16x16x32_bf16 v[112:115], v[24:27], v[40:43], v[88:91]
	v_mfma_f32_16x16x32_bf16 v[36:39], v[32:35], v[40:43], v[36:39]
	v_mfma_f32_16x16x32_bf16 v[40:43], v[20:23], v[44:47], 0
	v_mfma_f32_16x16x32_bf16 v[44:47], v[28:31], v[44:47], 0
	v_mfma_f32_16x16x32_bf16 v[40:43], v[24:27], v[48:51], v[40:43]
	v_mfma_f32_16x16x32_bf16 v[44:47], v[32:35], v[48:51], v[44:47]
	v_mfma_f32_16x16x32_bf16 v[48:51], v[20:23], v[52:55], 0
	v_mfma_f32_16x16x32_bf16 v[52:55], v[28:31], v[52:55], 0
	v_mfma_f32_16x16x32_bf16 v[48:51], v[24:27], v[56:59], v[48:51]
	v_mfma_f32_16x16x32_bf16 v[52:55], v[32:35], v[56:59], v[52:55]
	v_mfma_f32_16x16x32_bf16 v[56:59], v[20:23], v[60:63], 0
	v_mfma_f32_16x16x32_bf16 v[60:63], v[28:31], v[60:63], 0
	v_mfma_f32_16x16x32_bf16 v[56:59], v[24:27], v[64:67], v[56:59]
	v_mfma_f32_16x16x32_bf16 v[60:63], v[32:35], v[64:67], v[60:63]
	s_barrier
	v_lshl_add_u64 v[186:187], s[28:29], 0, v[132:133]
	s_mov_b64 s[10:11], 0x100
	s_add_i32 s45, s45, s36
	v_lshl_add_u64 v[142:143], v[186:187], 0, s[10:11]
	s_mov_b32 m0, s45
	s_mov_b64 s[48:49], 0x40100
	s_add_i32 s46, s45, 0x2000
	ds_read_b128 v[64:67], v163 offset:16384
	ds_read_b128 v[88:91], v163 offset:17408
	ds_read_b128 v[100:103], v163 offset:18432
	ds_read_b128 v[104:107], v163 offset:19456
	ds_read_b128 v[116:119], v163 offset:20480
	ds_read_b128 v[120:123], v163 offset:21504
	ds_read_b128 v[124:127], v163 offset:22528
	ds_read_b128 v[128:131], v163 offset:23552
	global_load_lds_dwordx4 v[142:143], off
	v_lshl_add_u64 v[142:143], v[186:187], 0, s[48:49]
	s_mov_b32 m0, s46
	s_mov_b64 s[48:49], 0x80100
	s_add_i32 s47, s47, s36
	global_load_lds_dwordx4 v[142:143], off
	v_lshl_add_u64 v[142:143], v[186:187], 0, s[48:49]
	s_mov_b32 m0, s47
	s_mov_b64 s[48:49], 0xc0100
	global_load_lds_dwordx4 v[142:143], off
	v_lshl_add_u64 v[142:143], v[186:187], 0, s[48:49]
	s_add_i32 s48, s47, 0x2000
	s_mov_b32 m0, s48
	s_nop 0
	global_load_lds_dwordx4 v[142:143], off
	v_lshl_add_u64 v[142:143], v[184:185], 0, s[10:11]
	s_mov_b32 m0, s37
	s_mov_b64 s[10:11], 0x42100
	global_load_lds_dwordx4 v[142:143], off
	v_lshl_add_u64 v[142:143], v[184:185], 0, s[10:11]
	s_mov_b32 m0, s38
	s_nop 0
	global_load_lds_dwordx4 v[142:143], off
	s_waitcnt vmcnt(16)
	s_waitcnt lgkmcnt(0)
	s_barrier
	s_waitcnt lgkmcnt(0)
	v_mfma_f32_16x16x32_bf16 v[142:145], v[4:7], v[64:67], 0
	v_mfma_f32_16x16x32_bf16 v[152:155], v[4:7], v[100:103], 0
	v_mfma_f32_16x16x32_bf16 v[164:167], v[4:7], v[116:119], 0
	v_mfma_f32_16x16x32_bf16 v[4:7], v[4:7], v[124:127], 0
	v_mfma_f32_16x16x32_bf16 v[144:147], v[8:11], v[88:91], v[142:145]
	v_mfma_f32_16x16x32_bf16 v[152:155], v[8:11], v[104:107], v[152:155]
	v_mfma_f32_16x16x32_bf16 v[164:167], v[8:11], v[120:123], v[164:167]
	v_mfma_f32_16x16x32_bf16 v[4:7], v[8:11], v[128:131], v[4:7]
	v_mfma_f32_16x16x32_bf16 v[8:11], v[12:15], v[124:127], 0
	v_mfma_f32_16x16x32_bf16 v[148:151], v[12:15], v[64:67], 0
	v_mfma_f32_16x16x32_bf16 v[156:159], v[12:15], v[100:103], 0
	v_mfma_f32_16x16x32_bf16 v[168:171], v[12:15], v[116:119], 0
	v_mfma_f32_16x16x32_bf16 v[12:15], v[16:19], v[128:131], v[8:11]
	v_mfma_f32_16x16x32_bf16 v[148:151], v[16:19], v[88:91], v[148:151]
	v_mfma_f32_16x16x32_bf16 v[156:159], v[16:19], v[104:107], v[156:159]
	v_mfma_f32_16x16x32_bf16 v[168:171], v[16:19], v[120:123], v[168:171]
	v_mfma_f32_16x16x32_bf16 v[8:11], v[20:23], v[64:67], 0
	v_mfma_f32_16x16x32_bf16 v[16:19], v[24:27], v[88:91], v[8:11]
	v_mfma_f32_16x16x32_bf16 v[8:11], v[28:31], v[64:67], 0
	v_mfma_f32_16x16x32_bf16 v[172:175], v[32:35], v[88:91], v[8:11]
	v_mfma_f32_16x16x32_bf16 v[8:11], v[20:23], v[100:103], 0
	v_mfma_f32_16x16x32_bf16 v[176:179], v[24:27], v[104:107], v[8:11]
	v_mfma_f32_16x16x32_bf16 v[8:11], v[28:31], v[100:103], 0
	v_mfma_f32_16x16x32_bf16 v[194:197], v[32:35], v[104:107], v[8:11]
	v_mfma_f32_16x16x32_bf16 v[8:11], v[20:23], v[116:119], 0
	v_mfma_f32_16x16x32_bf16 v[198:201], v[24:27], v[120:123], v[8:11]
	v_mfma_f32_16x16x32_bf16 v[8:11], v[28:31], v[116:119], 0
	v_mfma_f32_16x16x32_bf16 v[202:205], v[32:35], v[120:123], v[8:11]
	v_mfma_f32_16x16x32_bf16 v[8:11], v[20:23], v[124:127], 0
	v_mfma_f32_16x16x32_bf16 v[206:209], v[24:27], v[128:131], v[8:11]
	v_mfma_f32_16x16x32_bf16 v[8:11], v[28:31], v[124:127], 0
	v_mfma_f32_16x16x32_bf16 v[220:223], v[32:35], v[128:131], v[8:11]
	s_barrier
	s_add_i32 s49, 0, 0x18000
	s_add_i32 s51, 0, 0x1c000
	v_add_u32_e32 v142, s49, v160
	v_add_u32_e32 v143, s51, v160
	s_nop 0
	ds_read_b128 v[8:11], v142
	ds_read_b128 v[28:31], v142 offset:1024
	ds_read_b128 v[32:35], v142 offset:2048
	ds_read_b128 v[64:67], v142 offset:3072
	ds_read_b128 v[224:227], v143
	ds_read_b128 v[228:231], v143 offset:1024
	ds_read_b128 v[232:235], v143 offset:2048
	ds_read_b128 v[236:239], v143 offset:3072
	s_mov_b64 s[10:11], 0x84100
	s_mov_b32 m0, s39
	v_lshl_add_u64 v[88:89], v[184:185], 0, s[10:11]
	s_mov_b64 s[10:11], 0xc6100
	ds_read_b128 v[20:23], v163 offset:32768
	ds_read_b128 v[24:27], v163 offset:33792
	ds_read_b128 v[240:243], v163 offset:34816
	ds_read_b128 v[244:247], v163 offset:35840
	ds_read_b128 v[248:251], v163 offset:36864
	ds_read_b128 v[216:219], v163 offset:37888
	ds_read_b128 v[190:193], v163 offset:38912
	ds_read_b128 v[180:183], v163 offset:39936
	global_load_lds_dwordx4 v[88:89], off
	v_lshl_add_u64 v[88:89], v[184:185], 0, s[10:11]
	s_mov_b32 m0, s40
	s_nop 0
	global_load_lds_dwordx4 v[88:89], off
	s_waitcnt vmcnt(8)
	s_waitcnt lgkmcnt(0)
	s_barrier
	s_waitcnt lgkmcnt(0)
	v_mfma_f32_16x16x32_bf16 v[68:71], v[8:11], v[20:23], v[68:71]
	v_mfma_f32_16x16x32_bf16 v[120:123], v[28:31], v[24:27], v[68:71]
	v_mfma_f32_16x16x32_bf16 v[68:71], v[32:35], v[20:23], v[72:75]
	v_mfma_f32_16x16x32_bf16 v[116:119], v[64:67], v[24:27], v[68:71]
	v_mfma_f32_16x16x32_bf16 v[68:71], v[8:11], v[240:243], v[76:79]
	v_mfma_f32_16x16x32_bf16 v[104:107], v[28:31], v[244:247], v[68:71]
	v_mfma_f32_16x16x32_bf16 v[68:71], v[32:35], v[240:243], v[80:83]
	v_mfma_f32_16x16x32_bf16 v[100:103], v[64:67], v[244:247], v[68:71]
	v_mfma_f32_16x16x32_bf16 v[68:71], v[8:11], v[248:251], v[84:87]
	v_mfma_f32_16x16x32_bf16 v[88:91], v[28:31], v[216:219], v[68:71]
	v_mfma_f32_16x16x32_bf16 v[68:71], v[32:35], v[248:251], v[92:95]
	v_mfma_f32_16x16x32_bf16 v[84:87], v[64:67], v[216:219], v[68:71]
	v_mfma_f32_16x16x32_bf16 v[68:71], v[8:11], v[190:193], v[96:99]
	v_mfma_f32_16x16x32_bf16 v[72:75], v[28:31], v[180:183], v[68:71]
	v_mfma_f32_16x16x32_bf16 v[68:71], v[32:35], v[190:193], v[108:111]
	v_mfma_f32_16x16x32_bf16 v[68:71], v[64:67], v[180:183], v[68:71]
	v_mfma_f32_16x16x32_bf16 v[76:79], v[224:227], v[20:23], v[112:115]
	v_mfma_f32_16x16x32_bf16 v[20:23], v[232:235], v[20:23], v[36:39]
	v_mfma_f32_16x16x32_bf16 v[124:127], v[236:239], v[24:27], v[20:23]
	v_mfma_f32_16x16x32_bf16 v[20:23], v[224:227], v[240:243], v[40:43]
	v_mfma_f32_16x16x32_bf16 v[112:115], v[228:231], v[244:247], v[20:23]
	v_mfma_f32_16x16x32_bf16 v[20:23], v[232:235], v[240:243], v[44:47]
	v_mfma_f32_16x16x32_bf16 v[108:111], v[236:239], v[244:247], v[20:23]
	v_mfma_f32_16x16x32_bf16 v[20:23], v[224:227], v[248:251], v[48:51]
	v_mfma_f32_16x16x32_bf16 v[96:99], v[228:231], v[216:219], v[20:23]
	v_mfma_f32_16x16x32_bf16 v[20:23], v[232:235], v[248:251], v[52:55]
	v_mfma_f32_16x16x32_bf16 v[92:95], v[236:239], v[216:219], v[20:23]
	v_mfma_f32_16x16x32_bf16 v[20:23], v[224:227], v[190:193], v[56:59]
	v_mfma_f32_16x16x32_bf16 v[80:83], v[228:231], v[180:183], v[20:23]
	v_mfma_f32_16x16x32_bf16 v[20:23], v[232:235], v[190:193], v[60:63]
	v_mfma_f32_16x16x32_bf16 v[128:131], v[228:231], v[24:27], v[76:79]
	v_mfma_f32_16x16x32_bf16 v[76:79], v[236:239], v[180:183], v[20:23]
	s_barrier
; #define PG8_MMA(ai, bj, At, Bt) do { __builtin_amdgcn_s_setprio(1); _Pragma("unroll") for (int m = 0; m < 4; ++m) _Pragma("unroll") for (int n = 0; n < 2; ++n) _Pragma("unroll") for (int k = 0; k < 2; ++k) \
;         acc[ai][bj][m][n] = __builtin_amdgcn_mfma_f32_16x16x32_bf16(Bt[n][k], At[m][k], acc[ai][bj][m][n], 0, 0, 0); __builtin_amdgcn_s_setprio(0); } while (0)
; #define PG8_WAIT_V(n) asm volatile("s_waitcnt vmcnt(" #n ")" ::: "memory")
; #define PG8_TRIP_HEAD(T) const int t = (T); const bool last = (t == nt - 2); \
;             const char* a1 = cA + (size_t)(t + 1) * kstep; \
;             const char* a2 = last ? nA : cA + (size_t)(t + 2) * kstep; const char* b2 = last ? nB : cB + (size_t)(t + 2) * kstep; \
;             const char* a3 = a2 + kstep; const char* b3 = b2 + kstep; \
;             if (last && has_next) S.a_ready(nxt);
; template <class Epi, class Sched, bool ALIGN_EPI = false, bool SP2 = false>
; __device__ __forceinline__ void gemm_phase(PG8_LAS unsigned char* lds, const Gemm g, const Sched& S, const Epi& E) {
;     ...
;         if constexpr (SP2) {
;             { PG8_TRIP_HEAD(0) PG8_TRIP_SP2(asm volatile("s_waitcnt vmcnt(%0)" :: "n"(8 + Epi::NST) : "memory"), PG8_MMAZ) }
;             for (int tt = 2; tt < nt; tt += 2) { PG8_TRIP_HEAD(tt) PG8_TRIP_SP2(PG8_WAIT_V(8), PG8_MMA) }
	s_mov_b64 s[10:11], 0x180
	s_add_i32 s49, s49, s36
	s_nop 1
	v_lshl_add_u64 v[20:21], v[186:187], 0, s[10:11]
	s_mov_b32 m0, s49
	s_mov_b64 s[52:53], 0x40180
	s_add_i32 s50, s49, 0x2000
	ds_read_b128 v[44:47], v163 offset:49152
	ds_read_b128 v[48:51], v163 offset:50176
	ds_read_b128 v[180:183], v163 offset:51200
	ds_read_b128 v[190:193], v163 offset:52224
	ds_read_b128 v[216:219], v163 offset:53248
	ds_read_b128 v[240:243], v163 offset:54272
	ds_read_b128 v[244:247], v163 offset:55296
	ds_read_b128 v[248:251], v163 offset:56320
	global_load_lds_dwordx4 v[20:21], off
	v_lshl_add_u64 v[20:21], v[186:187], 0, s[52:53]
	s_mov_b32 m0, s50
	s_mov_b64 s[52:53], 0x80180
	s_add_i32 s51, s51, s36
	global_load_lds_dwordx4 v[20:21], off
	v_lshl_add_u64 v[20:21], v[186:187], 0, s[52:53]
	s_mov_b32 m0, s51
	s_mov_b64 s[52:53], 0xc0180
	global_load_lds_dwordx4 v[20:21], off
	v_lshl_add_u64 v[20:21], v[186:187], 0, s[52:53]
	s_add_i32 s52, s51, 0x2000
	s_mov_b32 m0, s52
	s_nop 0
	global_load_lds_dwordx4 v[20:21], off
	v_lshl_add_u64 v[20:21], v[184:185], 0, s[10:11]
	s_mov_b32 m0, s0
	s_mov_b64 s[10:11], 0x42180
	global_load_lds_dwordx4 v[20:21], off
	v_lshl_add_u64 v[20:21], v[184:185], 0, s[10:11]
	s_mov_b32 m0, s41
	s_nop 0
	global_load_lds_dwordx4 v[20:21], off
	s_waitcnt vmcnt(8)
	s_waitcnt lgkmcnt(0)
	s_barrier
	s_waitcnt lgkmcnt(0)
	v_mfma_f32_16x16x32_bf16 v[20:23], v[8:11], v[44:47], v[144:147]
	v_mfma_f32_16x16x32_bf16 v[56:59], v[28:31], v[48:51], v[20:23]
	v_mfma_f32_16x16x32_bf16 v[20:23], v[32:35], v[44:47], v[148:151]
	v_mfma_f32_16x16x32_bf16 v[52:55], v[64:67], v[48:51], v[20:23]
	v_mfma_f32_16x16x32_bf16 v[20:23], v[8:11], v[180:183], v[152:155]
	v_mfma_f32_16x16x32_bf16 v[40:43], v[28:31], v[190:193], v[20:23]
	v_mfma_f32_16x16x32_bf16 v[20:23], v[32:35], v[180:183], v[156:159]
	v_mfma_f32_16x16x32_bf16 v[36:39], v[64:67], v[190:193], v[20:23]
	v_mfma_f32_16x16x32_bf16 v[20:23], v[8:11], v[216:219], v[164:167]
	v_mfma_f32_16x16x32_bf16 v[4:7], v[8:11], v[244:247], v[4:7]
	v_mfma_f32_16x16x32_bf16 v[24:27], v[28:31], v[240:243], v[20:23]
	v_mfma_f32_16x16x32_bf16 v[20:23], v[32:35], v[216:219], v[168:171]
	v_mfma_f32_16x16x32_bf16 v[8:11], v[28:31], v[248:251], v[4:7]
	v_mfma_f32_16x16x32_bf16 v[4:7], v[32:35], v[244:247], v[12:15]
	v_mfma_f32_16x16x32_bf16 v[20:23], v[64:67], v[240:243], v[20:23]
	v_mfma_f32_16x16x32_bf16 v[4:7], v[64:67], v[248:251], v[4:7]
	v_mfma_f32_16x16x32_bf16 v[12:15], v[224:227], v[44:47], v[16:19]
	v_mfma_f32_16x16x32_bf16 v[64:67], v[228:231], v[48:51], v[12:15]
	v_mfma_f32_16x16x32_bf16 v[12:15], v[232:235], v[44:47], v[172:175]
	v_mfma_f32_16x16x32_bf16 v[60:63], v[236:239], v[48:51], v[12:15]
	v_mfma_f32_16x16x32_bf16 v[12:15], v[224:227], v[180:183], v[176:179]
	v_mfma_f32_16x16x32_bf16 v[48:51], v[228:231], v[190:193], v[12:15]
	v_mfma_f32_16x16x32_bf16 v[12:15], v[232:235], v[180:183], v[194:197]
	v_mfma_f32_16x16x32_bf16 v[44:47], v[236:239], v[190:193], v[12:15]
	v_mfma_f32_16x16x32_bf16 v[12:15], v[224:227], v[216:219], v[198:201]
	v_mfma_f32_16x16x32_bf16 v[32:35], v[228:231], v[240:243], v[12:15]
	v_mfma_f32_16x16x32_bf16 v[12:15], v[232:235], v[216:219], v[202:205]
	v_mfma_f32_16x16x32_bf16 v[28:31], v[236:239], v[240:243], v[12:15]
	v_mfma_f32_16x16x32_bf16 v[12:15], v[224:227], v[244:247], v[206:209]
	v_mfma_f32_16x16x32_bf16 v[16:19], v[228:231], v[248:251], v[12:15]
	v_mfma_f32_16x16x32_bf16 v[12:15], v[232:235], v[244:247], v[220:223]
	v_mfma_f32_16x16x32_bf16 v[12:15], v[236:239], v[248:251], v[12:15]
	s_barrier
	s_add_u32 s10, s30, 0x84180
	s_addc_u32 s11, s31, 0
	s_add_u32 s28, s28, 0x200
	s_addc_u32 s29, s29, 0
	s_mov_b32 s30, 0
	s_mov_b64 s[60:61], 0x80000
	s_mov_b64 s[62:63], 0x80080
	s_mov_b64 s[64:65], 0xc0000
	s_mov_b64 s[66:67], 0xc0080
	s_mov_b64 s[68:69], 0xc6000
.LBB0_130:
	ds_read_b128 v[144:147], v140
	ds_read_b128 v[148:151], v140 offset:1024
	ds_read_b128 v[152:155], v140 offset:2048
	ds_read_b128 v[156:159], v140 offset:3072
	ds_read_b128 v[164:167], v141
	ds_read_b128 v[168:171], v141 offset:1024
	ds_read_b128 v[172:175], v141 offset:2048
	ds_read_b128 v[176:179], v141 offset:3072
	s_add_u32 s31, s10, 0xfff7c080
	s_addc_u32 s53, s11, -1
	s_cmp_eq_u32 s30, 28
	s_cselect_b32 s55, s25, s53
	s_cselect_b32 s54, s24, s31
	s_cselect_b32 s57, s4, s29
	s_cselect_b32 s56, s5, s28
	s_mov_b32 m0, s23
	v_lshl_add_u64 v[184:185], s[10:11], 0, v[138:139]
	ds_read_b128 v[180:183], v163
	ds_read_b128 v[190:193], v163 offset:1024
	ds_read_b128 v[194:197], v163 offset:2048
	ds_read_b128 v[198:201], v163 offset:3072
	ds_read_b128 v[202:205], v163 offset:4096
	ds_read_b128 v[206:209], v163 offset:5120
	ds_read_b128 v[216:219], v163 offset:6144
	ds_read_b128 v[220:223], v163 offset:7168
	global_load_lds_dwordx4 v[184:185], off
	v_lshl_add_u64 v[184:185], v[184:185], 0, s[96:97]
	s_mov_b32 m0, s33
	s_nop 0
	global_load_lds_dwordx4 v[184:185], off
	s_waitcnt vmcnt(8)
	s_waitcnt lgkmcnt(0)
	s_barrier
	s_waitcnt lgkmcnt(0)
	v_mfma_f32_16x16x32_bf16 v[120:123], v[144:147], v[180:183], v[120:123]
	v_mfma_f32_16x16x32_bf16 v[120:123], v[148:151], v[190:193], v[120:123]
	v_mfma_f32_16x16x32_bf16 v[116:119], v[152:155], v[180:183], v[116:119]
	v_mfma_f32_16x16x32_bf16 v[116:119], v[156:159], v[190:193], v[116:119]
	v_mfma_f32_16x16x32_bf16 v[104:107], v[144:147], v[194:197], v[104:107]
	v_mfma_f32_16x16x32_bf16 v[104:107], v[148:151], v[198:201], v[104:107]
	v_mfma_f32_16x16x32_bf16 v[100:103], v[152:155], v[194:197], v[100:103]
	v_mfma_f32_16x16x32_bf16 v[100:103], v[156:159], v[198:201], v[100:103]
	v_mfma_f32_16x16x32_bf16 v[88:91], v[144:147], v[202:205], v[88:91]
	v_mfma_f32_16x16x32_bf16 v[88:91], v[148:151], v[206:209], v[88:91]
	v_mfma_f32_16x16x32_bf16 v[84:87], v[152:155], v[202:205], v[84:87]
	v_mfma_f32_16x16x32_bf16 v[84:87], v[156:159], v[206:209], v[84:87]
	v_mfma_f32_16x16x32_bf16 v[72:75], v[144:147], v[216:219], v[72:75]
	v_mfma_f32_16x16x32_bf16 v[72:75], v[148:151], v[220:223], v[72:75]
	v_mfma_f32_16x16x32_bf16 v[68:71], v[152:155], v[216:219], v[68:71]
	v_mfma_f32_16x16x32_bf16 v[68:71], v[156:159], v[220:223], v[68:71]
	v_mfma_f32_16x16x32_bf16 v[128:131], v[164:167], v[180:183], v[128:131]
	v_mfma_f32_16x16x32_bf16 v[128:131], v[168:171], v[190:193], v[128:131]
	v_mfma_f32_16x16x32_bf16 v[124:127], v[172:175], v[180:183], v[124:127]
	v_mfma_f32_16x16x32_bf16 v[124:127], v[176:179], v[190:193], v[124:127]
	v_mfma_f32_16x16x32_bf16 v[112:115], v[164:167], v[194:197], v[112:115]
	v_mfma_f32_16x16x32_bf16 v[112:115], v[168:171], v[198:201], v[112:115]
	v_mfma_f32_16x16x32_bf16 v[108:111], v[172:175], v[194:197], v[108:111]
	v_mfma_f32_16x16x32_bf16 v[108:111], v[176:179], v[198:201], v[108:111]
	v_mfma_f32_16x16x32_bf16 v[96:99], v[164:167], v[202:205], v[96:99]
	v_mfma_f32_16x16x32_bf16 v[96:99], v[168:171], v[206:209], v[96:99]
	v_mfma_f32_16x16x32_bf16 v[92:95], v[172:175], v[202:205], v[92:95]
	v_mfma_f32_16x16x32_bf16 v[92:95], v[176:179], v[206:209], v[92:95]
	v_mfma_f32_16x16x32_bf16 v[80:83], v[164:167], v[216:219], v[80:83]
	v_mfma_f32_16x16x32_bf16 v[80:83], v[168:171], v[220:223], v[80:83]
	v_mfma_f32_16x16x32_bf16 v[76:79], v[172:175], v[216:219], v[76:79]
	v_mfma_f32_16x16x32_bf16 v[76:79], v[176:179], v[220:223], v[76:79]
	s_barrier
	s_mov_b32 m0, s45
	v_lshl_add_u64 v[184:185], s[56:57], 0, v[132:133]
	ds_read_b128 v[180:183], v163 offset:16384
	ds_read_b128 v[190:193], v163 offset:17408
	ds_read_b128 v[194:197], v163 offset:18432
	ds_read_b128 v[198:201], v163 offset:19456
	ds_read_b128 v[202:205], v163 offset:20480
	ds_read_b128 v[206:209], v163 offset:21504
	ds_read_b128 v[216:219], v163 offset:22528
	ds_read_b128 v[220:223], v163 offset:23552
	global_load_lds_dwordx4 v[184:185], off
	v_lshl_add_u64 v[186:187], v[184:185], 0, s[90:91]
	s_mov_b32 m0, s46
	s_nop 0
	global_load_lds_dwordx4 v[186:187], off
	v_lshl_add_u64 v[186:187], v[184:185], 0, s[60:61]
	s_mov_b32 m0, s47
	s_nop 0
	global_load_lds_dwordx4 v[186:187], off
	v_lshl_add_u64 v[186:187], v[184:185], 0, s[64:65]
	s_mov_b32 m0, s48
	s_nop 0
	global_load_lds_dwordx4 v[186:187], off
	v_lshl_add_u64 v[186:187], s[54:55], 0, v[134:135]
	s_mov_b32 m0, s37
	v_lshl_add_u64 v[188:189], v[186:187], 0, s[96:97]
	global_load_lds_dwordx4 v[186:187], off
	s_mov_b32 m0, s38
	s_nop 0
	global_load_lds_dwordx4 v[188:189], off
	s_waitcnt vmcnt(8)
	s_waitcnt lgkmcnt(0)
	s_barrier
	s_waitcnt lgkmcnt(0)
	v_mfma_f32_16x16x32_bf16 v[56:59], v[144:147], v[180:183], v[56:59]
	v_mfma_f32_16x16x32_bf16 v[56:59], v[148:151], v[190:193], v[56:59]
	v_mfma_f32_16x16x32_bf16 v[52:55], v[152:155], v[180:183], v[52:55]
	v_mfma_f32_16x16x32_bf16 v[52:55], v[156:159], v[190:193], v[52:55]
	v_mfma_f32_16x16x32_bf16 v[40:43], v[144:147], v[194:197], v[40:43]
	v_mfma_f32_16x16x32_bf16 v[40:43], v[148:151], v[198:201], v[40:43]
	v_mfma_f32_16x16x32_bf16 v[36:39], v[152:155], v[194:197], v[36:39]
	v_mfma_f32_16x16x32_bf16 v[36:39], v[156:159], v[198:201], v[36:39]
	v_mfma_f32_16x16x32_bf16 v[24:27], v[144:147], v[202:205], v[24:27]
	v_mfma_f32_16x16x32_bf16 v[24:27], v[148:151], v[206:209], v[24:27]
	v_mfma_f32_16x16x32_bf16 v[20:23], v[152:155], v[202:205], v[20:23]
	v_mfma_f32_16x16x32_bf16 v[20:23], v[156:159], v[206:209], v[20:23]
	v_mfma_f32_16x16x32_bf16 v[8:11], v[144:147], v[216:219], v[8:11]
	v_mfma_f32_16x16x32_bf16 v[8:11], v[148:151], v[220:223], v[8:11]
	v_mfma_f32_16x16x32_bf16 v[4:7], v[152:155], v[216:219], v[4:7]
	v_mfma_f32_16x16x32_bf16 v[4:7], v[156:159], v[220:223], v[4:7]
	v_mfma_f32_16x16x32_bf16 v[64:67], v[164:167], v[180:183], v[64:67]
	v_mfma_f32_16x16x32_bf16 v[64:67], v[168:171], v[190:193], v[64:67]
	v_mfma_f32_16x16x32_bf16 v[60:63], v[172:175], v[180:183], v[60:63]
	v_mfma_f32_16x16x32_bf16 v[60:63], v[176:179], v[190:193], v[60:63]
	v_mfma_f32_16x16x32_bf16 v[48:51], v[164:167], v[194:197], v[48:51]
	v_mfma_f32_16x16x32_bf16 v[48:51], v[168:171], v[198:201], v[48:51]
	v_mfma_f32_16x16x32_bf16 v[44:47], v[172:175], v[194:197], v[44:47]
	v_mfma_f32_16x16x32_bf16 v[44:47], v[176:179], v[198:201], v[44:47]
	v_mfma_f32_16x16x32_bf16 v[32:35], v[164:167], v[202:205], v[32:35]
	v_mfma_f32_16x16x32_bf16 v[32:35], v[168:171], v[206:209], v[32:35]
	v_mfma_f32_16x16x32_bf16 v[28:31], v[172:175], v[202:205], v[28:31]
	v_mfma_f32_16x16x32_bf16 v[28:31], v[176:179], v[206:209], v[28:31]
	v_mfma_f32_16x16x32_bf16 v[16:19], v[164:167], v[216:219], v[16:19]
	v_mfma_f32_16x16x32_bf16 v[16:19], v[168:171], v[220:223], v[16:19]
	v_mfma_f32_16x16x32_bf16 v[12:15], v[172:175], v[216:219], v[12:15]
	v_mfma_f32_16x16x32_bf16 v[12:15], v[176:179], v[220:223], v[12:15]
	s_barrier
; #define PG8_MMA(ai, bj, At, Bt) do { __builtin_amdgcn_s_setprio(1); _Pragma("unroll") for (int m = 0; m < 4; ++m) _Pragma("unroll") for (int n = 0; n < 2; ++n) _Pragma("unroll") for (int k = 0; k < 2; ++k) \
;         acc[ai][bj][m][n] = __builtin_amdgcn_mfma_f32_16x16x32_bf16(Bt[n][k], At[m][k], acc[ai][bj][m][n], 0, 0, 0); __builtin_amdgcn_s_setprio(0); } while (0)
; #define PG8_WAIT_V(n) asm volatile("s_waitcnt vmcnt(" #n ")" ::: "memory")
; #define PG8_TRIP_HEAD(T) const int t = (T); const bool last = (t == nt - 2); \
;             const char* a1 = cA + (size_t)(t + 1) * kstep; \
;             const char* a2 = last ? nA : cA + (size_t)(t + 2) * kstep; const char* b2 = last ? nB : cB + (size_t)(t + 2) * kstep; \
;             const char* a3 = a2 + kstep; const char* b3 = b2 + kstep; \
;             if (last && has_next) S.a_ready(nxt);
; template <class Epi, class Sched, bool ALIGN_EPI = false, bool SP2 = false>
; __device__ __forceinline__ void gemm_phase(PG8_LAS unsigned char* lds, const Gemm g, const Sched& S, const Epi& E) {
;     ...
;         if constexpr (SP2) {
;             { PG8_TRIP_HEAD(0) PG8_TRIP_SP2(asm volatile("s_waitcnt vmcnt(%0)" :: "n"(8 + Epi::NST) : "memory"), PG8_MMAZ) }
;             for (int tt = 2; tt < nt; tt += 2) { PG8_TRIP_HEAD(tt) PG8_TRIP_SP2(PG8_WAIT_V(8), PG8_MMA) }
	ds_read_b128 v[144:147], v142
	ds_read_b128 v[148:151], v142 offset:1024
	ds_read_b128 v[152:155], v142 offset:2048
	ds_read_b128 v[156:159], v142 offset:3072
	ds_read_b128 v[164:167], v143
	ds_read_b128 v[168:171], v143 offset:1024
	ds_read_b128 v[172:175], v143 offset:2048
	ds_read_b128 v[176:179], v143 offset:3072
	s_mov_b32 m0, s39
	v_lshl_add_u64 v[188:189], v[186:187], 0, s[82:83]
	ds_read_b128 v[180:183], v163 offset:32768
	ds_read_b128 v[190:193], v163 offset:33792
	ds_read_b128 v[194:197], v163 offset:34816
	ds_read_b128 v[198:201], v163 offset:35840
	ds_read_b128 v[202:205], v163 offset:36864
	ds_read_b128 v[206:209], v163 offset:37888
	ds_read_b128 v[216:219], v163 offset:38912
	ds_read_b128 v[220:223], v163 offset:39936
	global_load_lds_dwordx4 v[188:189], off
	v_lshl_add_u64 v[188:189], v[186:187], 0, s[68:69]
	s_mov_b32 m0, s40
	s_nop 0
	global_load_lds_dwordx4 v[188:189], off
	s_waitcnt vmcnt(8)
	s_waitcnt lgkmcnt(0)
	s_barrier
	s_waitcnt lgkmcnt(0)
	v_mfma_f32_16x16x32_bf16 v[120:123], v[144:147], v[180:183], v[120:123]
	v_mfma_f32_16x16x32_bf16 v[120:123], v[148:151], v[190:193], v[120:123]
	v_mfma_f32_16x16x32_bf16 v[116:119], v[152:155], v[180:183], v[116:119]
	v_mfma_f32_16x16x32_bf16 v[116:119], v[156:159], v[190:193], v[116:119]
	v_mfma_f32_16x16x32_bf16 v[104:107], v[144:147], v[194:197], v[104:107]
	v_mfma_f32_16x16x32_bf16 v[104:107], v[148:151], v[198:201], v[104:107]
	v_mfma_f32_16x16x32_bf16 v[100:103], v[152:155], v[194:197], v[100:103]
	v_mfma_f32_16x16x32_bf16 v[100:103], v[156:159], v[198:201], v[100:103]
	v_mfma_f32_16x16x32_bf16 v[88:91], v[144:147], v[202:205], v[88:91]
	v_mfma_f32_16x16x32_bf16 v[88:91], v[148:151], v[206:209], v[88:91]
	v_mfma_f32_16x16x32_bf16 v[84:87], v[152:155], v[202:205], v[84:87]
	v_mfma_f32_16x16x32_bf16 v[84:87], v[156:159], v[206:209], v[84:87]
	v_mfma_f32_16x16x32_bf16 v[72:75], v[144:147], v[216:219], v[72:75]
	v_mfma_f32_16x16x32_bf16 v[72:75], v[148:151], v[220:223], v[72:75]
	v_mfma_f32_16x16x32_bf16 v[68:71], v[152:155], v[216:219], v[68:71]
	v_mfma_f32_16x16x32_bf16 v[68:71], v[156:159], v[220:223], v[68:71]
	v_mfma_f32_16x16x32_bf16 v[128:131], v[164:167], v[180:183], v[128:131]
	v_mfma_f32_16x16x32_bf16 v[128:131], v[168:171], v[190:193], v[128:131]
	v_mfma_f32_16x16x32_bf16 v[124:127], v[172:175], v[180:183], v[124:127]
	v_mfma_f32_16x16x32_bf16 v[124:127], v[176:179], v[190:193], v[124:127]
	v_mfma_f32_16x16x32_bf16 v[112:115], v[164:167], v[194:197], v[112:115]
	v_mfma_f32_16x16x32_bf16 v[112:115], v[168:171], v[198:201], v[112:115]
	v_mfma_f32_16x16x32_bf16 v[108:111], v[172:175], v[194:197], v[108:111]
	v_mfma_f32_16x16x32_bf16 v[108:111], v[176:179], v[198:201], v[108:111]
	v_mfma_f32_16x16x32_bf16 v[96:99], v[164:167], v[202:205], v[96:99]
	v_mfma_f32_16x16x32_bf16 v[96:99], v[168:171], v[206:209], v[96:99]
	v_mfma_f32_16x16x32_bf16 v[92:95], v[172:175], v[202:205], v[92:95]
	v_mfma_f32_16x16x32_bf16 v[92:95], v[176:179], v[206:209], v[92:95]
	v_mfma_f32_16x16x32_bf16 v[80:83], v[164:167], v[216:219], v[80:83]
	v_mfma_f32_16x16x32_bf16 v[80:83], v[168:171], v[220:223], v[80:83]
	v_mfma_f32_16x16x32_bf16 v[76:79], v[172:175], v[216:219], v[76:79]
	v_mfma_f32_16x16x32_bf16 v[76:79], v[176:179], v[220:223], v[76:79]
	s_barrier
	s_mov_b32 m0, s49
	v_lshl_add_u64 v[188:189], v[184:185], 0, s[78:79]
	ds_read_b128 v[180:183], v163 offset:49152
	ds_read_b128 v[190:193], v163 offset:50176
	ds_read_b128 v[194:197], v163 offset:51200
	ds_read_b128 v[198:201], v163 offset:52224
	ds_read_b128 v[202:205], v163 offset:53248
	ds_read_b128 v[206:209], v163 offset:54272
	ds_read_b128 v[216:219], v163 offset:55296
	ds_read_b128 v[220:223], v163 offset:56320
	global_load_lds_dwordx4 v[188:189], off
	v_lshl_add_u64 v[188:189], v[184:185], 0, s[84:85]
	s_mov_b32 m0, s50
	s_nop 0
	global_load_lds_dwordx4 v[188:189], off
	v_lshl_add_u64 v[188:189], v[184:185], 0, s[62:63]
	s_mov_b32 m0, s51
	v_lshl_add_u64 v[184:185], v[184:185], 0, s[66:67]
	global_load_lds_dwordx4 v[188:189], off
	s_mov_b32 m0, s52
	s_nop 0
	global_load_lds_dwordx4 v[184:185], off
	v_lshl_add_u64 v[184:185], v[186:187], 0, s[78:79]
	s_mov_b32 m0, s0
	s_nop 0
	global_load_lds_dwordx4 v[184:185], off
	v_lshl_add_u64 v[184:185], v[186:187], 0, s[92:93]
	s_mov_b32 m0, s41
	s_nop 0
	global_load_lds_dwordx4 v[184:185], off
	s_waitcnt vmcnt(8)
	s_waitcnt lgkmcnt(0)
	s_barrier
	s_waitcnt lgkmcnt(0)
	v_mfma_f32_16x16x32_bf16 v[56:59], v[144:147], v[180:183], v[56:59]
	v_mfma_f32_16x16x32_bf16 v[56:59], v[148:151], v[190:193], v[56:59]
	v_mfma_f32_16x16x32_bf16 v[52:55], v[152:155], v[180:183], v[52:55]
	v_mfma_f32_16x16x32_bf16 v[52:55], v[156:159], v[190:193], v[52:55]
	v_mfma_f32_16x16x32_bf16 v[40:43], v[144:147], v[194:197], v[40:43]
	v_mfma_f32_16x16x32_bf16 v[40:43], v[148:151], v[198:201], v[40:43]
	v_mfma_f32_16x16x32_bf16 v[36:39], v[152:155], v[194:197], v[36:39]
	v_mfma_f32_16x16x32_bf16 v[36:39], v[156:159], v[198:201], v[36:39]
	v_mfma_f32_16x16x32_bf16 v[24:27], v[144:147], v[202:205], v[24:27]
	v_mfma_f32_16x16x32_bf16 v[24:27], v[148:151], v[206:209], v[24:27]
	v_mfma_f32_16x16x32_bf16 v[20:23], v[152:155], v[202:205], v[20:23]
	v_mfma_f32_16x16x32_bf16 v[20:23], v[156:159], v[206:209], v[20:23]
	v_mfma_f32_16x16x32_bf16 v[8:11], v[144:147], v[216:219], v[8:11]
	v_mfma_f32_16x16x32_bf16 v[8:11], v[148:151], v[220:223], v[8:11]
	v_mfma_f32_16x16x32_bf16 v[4:7], v[152:155], v[216:219], v[4:7]
	v_mfma_f32_16x16x32_bf16 v[4:7], v[156:159], v[220:223], v[4:7]
	v_mfma_f32_16x16x32_bf16 v[64:67], v[164:167], v[180:183], v[64:67]
	v_mfma_f32_16x16x32_bf16 v[64:67], v[168:171], v[190:193], v[64:67]
	v_mfma_f32_16x16x32_bf16 v[60:63], v[172:175], v[180:183], v[60:63]
	v_mfma_f32_16x16x32_bf16 v[60:63], v[176:179], v[190:193], v[60:63]
	v_mfma_f32_16x16x32_bf16 v[48:51], v[164:167], v[194:197], v[48:51]
	v_mfma_f32_16x16x32_bf16 v[48:51], v[168:171], v[198:201], v[48:51]
	v_mfma_f32_16x16x32_bf16 v[44:47], v[172:175], v[194:197], v[44:47]
	v_mfma_f32_16x16x32_bf16 v[44:47], v[176:179], v[198:201], v[44:47]
	v_mfma_f32_16x16x32_bf16 v[32:35], v[164:167], v[202:205], v[32:35]
	v_mfma_f32_16x16x32_bf16 v[32:35], v[168:171], v[206:209], v[32:35]
	v_mfma_f32_16x16x32_bf16 v[28:31], v[172:175], v[202:205], v[28:31]
	v_mfma_f32_16x16x32_bf16 v[28:31], v[176:179], v[206:209], v[28:31]
	v_mfma_f32_16x16x32_bf16 v[16:19], v[164:167], v[216:219], v[16:19]
	v_mfma_f32_16x16x32_bf16 v[16:19], v[168:171], v[220:223], v[16:19]
	v_mfma_f32_16x16x32_bf16 v[12:15], v[172:175], v[216:219], v[12:15]
	v_mfma_f32_16x16x32_bf16 v[12:15], v[176:179], v[220:223], v[12:15]
	s_barrier
	s_add_i32 s30, s30, 2
	s_add_u32 s10, s10, 0x100
	s_addc_u32 s11, s11, 0
	s_add_u32 s28, s28, 0x100
	s_addc_u32 s29, s29, 0
	s_cmp_gt_u32 s30, 29
	s_cbranch_scc0 .LBB0_130
	s_and_b64 vcc, exec, s[20:21]
	s_cbranch_vccz .LBB0_133
	s_barrier

;     __device__ bool next(int i, Unit& u) const { const int rounds = nwg / G; if (i >= rounds) return false; return StaticOrder::next(rounds - 1 - i, u); }
;     __device__ bool next(int i, Unit& u) const { const int rounds = nwg / G; if (i >= 2 * rounds) return false; const bool ok = StaticOrder::next(i >= rounds ? i - rounds : i, u); u.z = (i >= rounds) ? 1 : 0; return ok; }
; template <class Epi, class Sched, bool ALIGN_EPI = false, bool SP2 = false>
; __device__ __forceinline__ void gemm_phase(PG8_LAS unsigned char* lds, const Gemm g, const Sched& S, const Epi& E) {
;     ...
;         const bool has_next = S.next(ui + 1, nxt);
;         const char* nA = has_next ? (const char*)S.opA(g, nxt) + (size_t)nxt.pm * tstepA : cA; const char* nB = has_next ? (const char*)S.opB(g, nxt) + (size_t)nxt.pn * tstepB : cB;
.LBB0_233:
	ds_read_b128 v[120:123], v116
	ds_read_b128 v[132:135], v116 offset:1024
	ds_read_b128 v[144:147], v116 offset:2048
	ds_read_b128 v[148:151], v116 offset:3072
	ds_read_b128 v[152:155], v117
	ds_read_b128 v[156:159], v117 offset:1024
	ds_read_b128 v[166:169], v117 offset:2048
	ds_read_b128 v[170:173], v117 offset:3072
	s_add_u32 s49, s26, 0xffea0080
	s_addc_u32 s50, s27, -1
	s_cmpk_eq_i32 s48, 0x54
	s_cselect_b32 s51, s21, s50
	s_cselect_b32 s50, s20, s49
	s_cselect_b32 s53, s23, s25
	s_cselect_b32 s52, s22, s24
	s_mov_b32 m0, s0
	v_lshl_add_u64 v[188:189], s[26:27], 0, v[164:165]
	ds_read_b128 v[180:183], v178
	ds_read_b128 v[184:187], v178 offset:1024
	ds_read_b128 v[190:193], v178 offset:2048
	ds_read_b128 v[194:197], v178 offset:3072
	ds_read_b128 v[198:201], v178 offset:4096
	ds_read_b128 v[202:205], v178 offset:5120
	ds_read_b128 v[206:209], v178 offset:6144
	ds_read_b128 v[216:219], v178 offset:7168
	global_load_lds_dwordx4 v[188:189], off
	v_lshl_add_u64 v[188:189], v[188:189], 0, s[86:87]
	s_mov_b32 m0, s4
	s_nop 0
	global_load_lds_dwordx4 v[188:189], off
	s_waitcnt vmcnt(8)
	s_waitcnt lgkmcnt(0)
	s_barrier
	s_waitcnt lgkmcnt(0)
	v_mfma_f32_16x16x32_bf16 v[140:143], v[120:123], v[180:183], v[140:143]
	v_mfma_f32_16x16x32_bf16 v[140:143], v[132:135], v[184:187], v[140:143]
	v_mfma_f32_16x16x32_bf16 v[136:139], v[144:147], v[180:183], v[136:139]
	v_mfma_f32_16x16x32_bf16 v[136:139], v[148:151], v[184:187], v[136:139]
	v_mfma_f32_16x16x32_bf16 v[112:115], v[120:123], v[190:193], v[112:115]
	v_mfma_f32_16x16x32_bf16 v[112:115], v[132:135], v[194:197], v[112:115]
	v_mfma_f32_16x16x32_bf16 v[108:111], v[144:147], v[190:193], v[108:111]
	v_mfma_f32_16x16x32_bf16 v[108:111], v[148:151], v[194:197], v[108:111]
	v_mfma_f32_16x16x32_bf16 v[96:99], v[120:123], v[198:201], v[96:99]
	v_mfma_f32_16x16x32_bf16 v[96:99], v[132:135], v[202:205], v[96:99]
	v_mfma_f32_16x16x32_bf16 v[92:95], v[144:147], v[198:201], v[92:95]
	v_mfma_f32_16x16x32_bf16 v[92:95], v[148:151], v[202:205], v[92:95]
	v_mfma_f32_16x16x32_bf16 v[80:83], v[120:123], v[206:209], v[80:83]
	v_mfma_f32_16x16x32_bf16 v[80:83], v[132:135], v[216:219], v[80:83]
	v_mfma_f32_16x16x32_bf16 v[76:79], v[144:147], v[206:209], v[76:79]
	v_mfma_f32_16x16x32_bf16 v[76:79], v[148:151], v[216:219], v[76:79]
	v_mfma_f32_16x16x32_bf16 v[128:131], v[152:155], v[180:183], v[128:131]
	v_mfma_f32_16x16x32_bf16 v[128:131], v[156:159], v[184:187], v[128:131]
	v_mfma_f32_16x16x32_bf16 v[124:127], v[166:169], v[180:183], v[124:127]
	v_mfma_f32_16x16x32_bf16 v[124:127], v[170:173], v[184:187], v[124:127]
	v_mfma_f32_16x16x32_bf16 v[104:107], v[152:155], v[190:193], v[104:107]
	v_mfma_f32_16x16x32_bf16 v[104:107], v[156:159], v[194:197], v[104:107]
	v_mfma_f32_16x16x32_bf16 v[100:103], v[166:169], v[190:193], v[100:103]
	v_mfma_f32_16x16x32_bf16 v[100:103], v[170:173], v[194:197], v[100:103]
	v_mfma_f32_16x16x32_bf16 v[88:91], v[152:155], v[198:201], v[88:91]
	v_mfma_f32_16x16x32_bf16 v[88:91], v[156:159], v[202:205], v[88:91]
	v_mfma_f32_16x16x32_bf16 v[84:87], v[166:169], v[198:201], v[84:87]
	v_mfma_f32_16x16x32_bf16 v[84:87], v[170:173], v[202:205], v[84:87]
	v_mfma_f32_16x16x32_bf16 v[72:75], v[152:155], v[206:209], v[72:75]
	v_mfma_f32_16x16x32_bf16 v[72:75], v[156:159], v[216:219], v[72:75]
	v_mfma_f32_16x16x32_bf16 v[68:71], v[166:169], v[206:209], v[68:71]
	v_mfma_f32_16x16x32_bf16 v[68:71], v[170:173], v[216:219], v[68:71]
	s_barrier
	s_mov_b32 m0, s5
	v_lshl_add_u64 v[188:189], s[52:53], 0, v[162:163]
	ds_read_b128 v[180:183], v178 offset:16384
	ds_read_b128 v[184:187], v178 offset:17408
	ds_read_b128 v[190:193], v178 offset:18432
	ds_read_b128 v[194:197], v178 offset:19456
	ds_read_b128 v[198:201], v178 offset:20480
	ds_read_b128 v[202:205], v178 offset:21504
	ds_read_b128 v[206:209], v178 offset:22528
	ds_read_b128 v[216:219], v178 offset:23552
	global_load_lds_dwordx4 v[188:189], off
	v_lshl_add_u64 v[214:215], v[188:189], 0, s[86:87]
	s_mov_b32 m0, s33
	s_nop 0
	global_load_lds_dwordx4 v[214:215], off
	v_lshl_add_u64 v[214:215], v[188:189], 0, s[54:55]
	s_mov_b32 m0, s42
	s_nop 0
	global_load_lds_dwordx4 v[214:215], off
	v_lshl_add_u64 v[214:215], v[188:189], 0, s[56:57]
	s_mov_b32 m0, s43
	s_nop 0
	global_load_lds_dwordx4 v[214:215], off
	v_lshl_add_u64 v[214:215], s[50:51], 0, v[160:161]
	s_mov_b32 m0, s31
	v_lshl_add_u64 v[220:221], v[214:215], 0, s[86:87]
	global_load_lds_dwordx4 v[214:215], off
	s_mov_b32 m0, s34
	s_nop 0
	global_load_lds_dwordx4 v[220:221], off
	s_waitcnt vmcnt(8)
	s_waitcnt lgkmcnt(0)
	s_barrier
	s_waitcnt lgkmcnt(0)
	v_mfma_f32_16x16x32_bf16 v[56:59], v[120:123], v[180:183], v[56:59]
	v_mfma_f32_16x16x32_bf16 v[56:59], v[132:135], v[184:187], v[56:59]
	v_mfma_f32_16x16x32_bf16 v[52:55], v[144:147], v[180:183], v[52:55]
	v_mfma_f32_16x16x32_bf16 v[52:55], v[148:151], v[184:187], v[52:55]
	v_mfma_f32_16x16x32_bf16 v[48:51], v[120:123], v[190:193], v[48:51]
	v_mfma_f32_16x16x32_bf16 v[48:51], v[132:135], v[194:197], v[48:51]
	v_mfma_f32_16x16x32_bf16 v[44:47], v[144:147], v[190:193], v[44:47]
	v_mfma_f32_16x16x32_bf16 v[44:47], v[148:151], v[194:197], v[44:47]
	v_mfma_f32_16x16x32_bf16 v[32:35], v[120:123], v[198:201], v[32:35]
	v_mfma_f32_16x16x32_bf16 v[32:35], v[132:135], v[202:205], v[32:35]
	v_mfma_f32_16x16x32_bf16 v[28:31], v[144:147], v[198:201], v[28:31]
	v_mfma_f32_16x16x32_bf16 v[28:31], v[148:151], v[202:205], v[28:31]
	v_mfma_f32_16x16x32_bf16 v[16:19], v[120:123], v[206:209], v[16:19]
	v_mfma_f32_16x16x32_bf16 v[16:19], v[132:135], v[216:219], v[16:19]
	v_mfma_f32_16x16x32_bf16 v[12:15], v[144:147], v[206:209], v[12:15]
	v_mfma_f32_16x16x32_bf16 v[12:15], v[148:151], v[216:219], v[12:15]
	v_mfma_f32_16x16x32_bf16 v[64:67], v[152:155], v[180:183], v[64:67]
	v_mfma_f32_16x16x32_bf16 v[64:67], v[156:159], v[184:187], v[64:67]
	v_mfma_f32_16x16x32_bf16 v[60:63], v[166:169], v[180:183], v[60:63]
	v_mfma_f32_16x16x32_bf16 v[60:63], v[170:173], v[184:187], v[60:63]
	v_mfma_f32_16x16x32_bf16 v[40:43], v[152:155], v[190:193], v[40:43]
	v_mfma_f32_16x16x32_bf16 v[40:43], v[156:159], v[194:197], v[40:43]
	v_mfma_f32_16x16x32_bf16 v[36:39], v[166:169], v[190:193], v[36:39]
	v_mfma_f32_16x16x32_bf16 v[36:39], v[170:173], v[194:197], v[36:39]
	v_mfma_f32_16x16x32_bf16 v[24:27], v[152:155], v[198:201], v[24:27]
	v_mfma_f32_16x16x32_bf16 v[24:27], v[156:159], v[202:205], v[24:27]
	v_mfma_f32_16x16x32_bf16 v[20:23], v[166:169], v[198:201], v[20:23]
	v_mfma_f32_16x16x32_bf16 v[20:23], v[170:173], v[202:205], v[20:23]
	v_mfma_f32_16x16x32_bf16 v[8:11], v[152:155], v[206:209], v[8:11]
	v_mfma_f32_16x16x32_bf16 v[8:11], v[156:159], v[216:219], v[8:11]
	v_mfma_f32_16x16x32_bf16 v[4:7], v[166:169], v[206:209], v[4:7]
	v_mfma_f32_16x16x32_bf16 v[4:7], v[170:173], v[216:219], v[4:7]
	s_barrier
	ds_read_b128 v[120:123], v118
	ds_read_b128 v[132:135], v118 offset:1024
	ds_read_b128 v[144:147], v118 offset:2048
	ds_read_b128 v[148:151], v118 offset:3072
	ds_read_b128 v[152:155], v119
	ds_read_b128 v[156:159], v119 offset:1024
	ds_read_b128 v[166:169], v119 offset:2048
	ds_read_b128 v[170:173], v119 offset:3072
	s_mov_b32 m0, s35
	v_lshl_add_u64 v[220:221], v[214:215], 0, s[54:55]
	ds_read_b128 v[180:183], v178 offset:32768
	ds_read_b128 v[184:187], v178 offset:33792
	ds_read_b128 v[190:193], v178 offset:34816
	ds_read_b128 v[194:197], v178 offset:35840
	ds_read_b128 v[198:201], v178 offset:36864
	ds_read_b128 v[202:205], v178 offset:37888
	ds_read_b128 v[206:209], v178 offset:38912
	ds_read_b128 v[216:219], v178 offset:39936
	global_load_lds_dwordx4 v[220:221], off
	v_lshl_add_u64 v[220:221], v[214:215], 0, s[56:57]
	s_mov_b32 m0, s36
	s_nop 0
	global_load_lds_dwordx4 v[220:221], off
	s_waitcnt vmcnt(8)
	s_waitcnt lgkmcnt(0)
	s_barrier
	s_waitcnt lgkmcnt(0)
	v_mfma_f32_16x16x32_bf16 v[140:143], v[120:123], v[180:183], v[140:143]
	v_mfma_f32_16x16x32_bf16 v[140:143], v[132:135], v[184:187], v[140:143]
	v_mfma_f32_16x16x32_bf16 v[136:139], v[144:147], v[180:183], v[136:139]
	v_mfma_f32_16x16x32_bf16 v[136:139], v[148:151], v[184:187], v[136:139]
	v_mfma_f32_16x16x32_bf16 v[112:115], v[120:123], v[190:193], v[112:115]
	v_mfma_f32_16x16x32_bf16 v[112:115], v[132:135], v[194:197], v[112:115]
	v_mfma_f32_16x16x32_bf16 v[108:111], v[144:147], v[190:193], v[108:111]
	v_mfma_f32_16x16x32_bf16 v[108:111], v[148:151], v[194:197], v[108:111]
	v_mfma_f32_16x16x32_bf16 v[96:99], v[120:123], v[198:201], v[96:99]
	v_mfma_f32_16x16x32_bf16 v[96:99], v[132:135], v[202:205], v[96:99]
	v_mfma_f32_16x16x32_bf16 v[92:95], v[144:147], v[198:201], v[92:95]
	v_mfma_f32_16x16x32_bf16 v[92:95], v[148:151], v[202:205], v[92:95]
	v_mfma_f32_16x16x32_bf16 v[80:83], v[120:123], v[206:209], v[80:83]
	v_mfma_f32_16x16x32_bf16 v[80:83], v[132:135], v[216:219], v[80:83]
	v_mfma_f32_16x16x32_bf16 v[76:79], v[144:147], v[206:209], v[76:79]
	v_mfma_f32_16x16x32_bf16 v[76:79], v[148:151], v[216:219], v[76:79]
	v_mfma_f32_16x16x32_bf16 v[128:131], v[152:155], v[180:183], v[128:131]
	v_mfma_f32_16x16x32_bf16 v[128:131], v[156:159], v[184:187], v[128:131]
	v_mfma_f32_16x16x32_bf16 v[124:127], v[166:169], v[180:183], v[124:127]
	v_mfma_f32_16x16x32_bf16 v[124:127], v[170:173], v[184:187], v[124:127]
	v_mfma_f32_16x16x32_bf16 v[104:107], v[152:155], v[190:193], v[104:107]
	v_mfma_f32_16x16x32_bf16 v[104:107], v[156:159], v[194:197], v[104:107]
	v_mfma_f32_16x16x32_bf16 v[100:103], v[166:169], v[190:193], v[100:103]
	v_mfma_f32_16x16x32_bf16 v[100:103], v[170:173], v[194:197], v[100:103]
	v_mfma_f32_16x16x32_bf16 v[88:91], v[152:155], v[198:201], v[88:91]
	v_mfma_f32_16x16x32_bf16 v[88:91], v[156:159], v[202:205], v[88:91]
	v_mfma_f32_16x16x32_bf16 v[84:87], v[166:169], v[198:201], v[84:87]
	v_mfma_f32_16x16x32_bf16 v[84:87], v[170:173], v[202:205], v[84:87]
	v_mfma_f32_16x16x32_bf16 v[72:75], v[152:155], v[206:209], v[72:75]
	v_mfma_f32_16x16x32_bf16 v[72:75], v[156:159], v[216:219], v[72:75]
	v_mfma_f32_16x16x32_bf16 v[68:71], v[166:169], v[206:209], v[68:71]
	v_mfma_f32_16x16x32_bf16 v[68:71], v[170:173], v[216:219], v[68:71]
	s_barrier
; #define PG8_MMA(ai, bj, At, Bt) do { __builtin_amdgcn_s_setprio(1); _Pragma("unroll") for (int m = 0; m < 4; ++m) _Pragma("unroll") for (int n = 0; n < 2; ++n) _Pragma("unroll") for (int k = 0; k < 2; ++k) \
;         acc[ai][bj][m][n] = __builtin_amdgcn_mfma_f32_16x16x32_bf16(Bt[n][k], At[m][k], acc[ai][bj][m][n], 0, 0, 0); __builtin_amdgcn_s_setprio(0); } while (0)
; #define PG8_WAIT_V(n) asm volatile("s_waitcnt vmcnt(" #n ")" ::: "memory")
; #define PG8_TRIP_HEAD(T) const int t = (T); const bool last = (t == nt - 2); \
;             const char* a1 = cA + (size_t)(t + 1) * kstep; \
;             const char* a2 = last ? nA : cA + (size_t)(t + 2) * kstep; const char* b2 = last ? nB : cB + (size_t)(t + 2) * kstep; \
;             const char* a3 = a2 + kstep; const char* b3 = b2 + kstep; \
;             if (last && has_next) S.a_ready(nxt);
; template <class Epi, class Sched, bool ALIGN_EPI = false, bool SP2 = false>
; __device__ __forceinline__ void gemm_phase(PG8_LAS unsigned char* lds, const Gemm g, const Sched& S, const Epi& E) {
;     ...
;         if constexpr (SP2) {
;             { PG8_TRIP_HEAD(0) PG8_TRIP_SP2(asm volatile("s_waitcnt vmcnt(%0)" :: "n"(8 + Epi::NST) : "memory"), PG8_MMAZ) }
;             for (int tt = 2; tt < nt; tt += 2) { PG8_TRIP_HEAD(tt) PG8_TRIP_SP2(PG8_WAIT_V(8), PG8_MMA) }
	s_mov_b32 m0, s44
	v_lshl_add_u64 v[220:221], v[188:189], 0, s[78:79]
	ds_read_b128 v[180:183], v178 offset:49152
	ds_read_b128 v[184:187], v178 offset:50176
	ds_read_b128 v[190:193], v178 offset:51200
	ds_read_b128 v[194:197], v178 offset:52224
	ds_read_b128 v[198:201], v178 offset:53248
	ds_read_b128 v[202:205], v178 offset:54272
	ds_read_b128 v[206:209], v178 offset:55296
	ds_read_b128 v[216:219], v178 offset:56320
	global_load_lds_dwordx4 v[220:221], off
	v_lshl_add_u64 v[220:221], v[188:189], 0, s[60:61]
	s_mov_b32 m0, s45
	s_nop 0
	global_load_lds_dwordx4 v[220:221], off
	v_lshl_add_u64 v[220:221], v[188:189], 0, s[62:63]
	s_mov_b32 m0, s46
	v_lshl_add_u64 v[188:189], v[188:189], 0, s[64:65]
	global_load_lds_dwordx4 v[220:221], off
	s_mov_b32 m0, s47
	s_nop 0
	global_load_lds_dwordx4 v[188:189], off
	v_lshl_add_u64 v[188:189], v[214:215], 0, s[78:79]
	s_mov_b32 m0, s37
	s_nop 0
	global_load_lds_dwordx4 v[188:189], off
	v_lshl_add_u64 v[188:189], v[214:215], 0, s[60:61]
	s_mov_b32 m0, s38
	s_nop 0
	global_load_lds_dwordx4 v[188:189], off
	s_waitcnt vmcnt(8)
	s_waitcnt lgkmcnt(0)
	s_barrier
	s_waitcnt lgkmcnt(0)
	v_mfma_f32_16x16x32_bf16 v[56:59], v[120:123], v[180:183], v[56:59]
	v_mfma_f32_16x16x32_bf16 v[56:59], v[132:135], v[184:187], v[56:59]
	v_mfma_f32_16x16x32_bf16 v[52:55], v[144:147], v[180:183], v[52:55]
	v_mfma_f32_16x16x32_bf16 v[52:55], v[148:151], v[184:187], v[52:55]
	v_mfma_f32_16x16x32_bf16 v[48:51], v[120:123], v[190:193], v[48:51]
	v_mfma_f32_16x16x32_bf16 v[48:51], v[132:135], v[194:197], v[48:51]
	v_mfma_f32_16x16x32_bf16 v[44:47], v[144:147], v[190:193], v[44:47]
	v_mfma_f32_16x16x32_bf16 v[44:47], v[148:151], v[194:197], v[44:47]
	v_mfma_f32_16x16x32_bf16 v[32:35], v[120:123], v[198:201], v[32:35]
	v_mfma_f32_16x16x32_bf16 v[32:35], v[132:135], v[202:205], v[32:35]
	v_mfma_f32_16x16x32_bf16 v[28:31], v[144:147], v[198:201], v[28:31]
	v_mfma_f32_16x16x32_bf16 v[28:31], v[148:151], v[202:205], v[28:31]
	v_mfma_f32_16x16x32_bf16 v[16:19], v[120:123], v[206:209], v[16:19]
	v_mfma_f32_16x16x32_bf16 v[16:19], v[132:135], v[216:219], v[16:19]
	v_mfma_f32_16x16x32_bf16 v[12:15], v[144:147], v[206:209], v[12:15]
	v_mfma_f32_16x16x32_bf16 v[12:15], v[148:151], v[216:219], v[12:15]
	v_mfma_f32_16x16x32_bf16 v[64:67], v[152:155], v[180:183], v[64:67]
	v_mfma_f32_16x16x32_bf16 v[64:67], v[156:159], v[184:187], v[64:67]
	v_mfma_f32_16x16x32_bf16 v[60:63], v[166:169], v[180:183], v[60:63]
	v_mfma_f32_16x16x32_bf16 v[60:63], v[170:173], v[184:187], v[60:63]
	v_mfma_f32_16x16x32_bf16 v[40:43], v[152:155], v[190:193], v[40:43]
	v_mfma_f32_16x16x32_bf16 v[40:43], v[156:159], v[194:197], v[40:43]
	v_mfma_f32_16x16x32_bf16 v[36:39], v[166:169], v[190:193], v[36:39]
	v_mfma_f32_16x16x32_bf16 v[36:39], v[170:173], v[194:197], v[36:39]
	v_mfma_f32_16x16x32_bf16 v[24:27], v[152:155], v[198:201], v[24:27]
	v_mfma_f32_16x16x32_bf16 v[24:27], v[156:159], v[202:205], v[24:27]
	v_mfma_f32_16x16x32_bf16 v[20:23], v[166:169], v[198:201], v[20:23]
	v_mfma_f32_16x16x32_bf16 v[20:23], v[170:173], v[202:205], v[20:23]
	v_mfma_f32_16x16x32_bf16 v[8:11], v[152:155], v[206:209], v[8:11]
	v_mfma_f32_16x16x32_bf16 v[8:11], v[156:159], v[216:219], v[8:11]
	v_mfma_f32_16x16x32_bf16 v[4:7], v[166:169], v[206:209], v[4:7]
	v_mfma_f32_16x16x32_bf16 v[4:7], v[170:173], v[216:219], v[4:7]
	s_barrier
	s_add_i32 s48, s48, 2
	s_add_u32 s26, s26, 0x100
	s_addc_u32 s27, s27, 0
	s_add_u32 s24, s24, 0x100
	s_addc_u32 s25, s25, 0
	s_cmpk_gt_u32 s48, 0x55
	s_cbranch_scc0 .LBB0_233
	s_and_b64 vcc, exec, s[18:19]
	s_cbranch_vccz .LBB0_236
	s_barrier

;     __device__ bool next(int i, Unit& u) const { const int rounds = nwg / G; if (i >= rounds) return false; return StaticOrder::next(rounds - 1 - i, u); }
;     __device__ bool next(int i, Unit& u) const { const int rounds = nwg / G; if (i >= 2 * rounds) return false; const bool ok = StaticOrder::next(i >= rounds ? i - rounds : i, u); u.z = (i >= rounds) ? 1 : 0; return ok; }
; template <class Epi, class Sched, bool ALIGN_EPI = false, bool SP2 = false>
; __device__ __forceinline__ void gemm_phase(PG8_LAS unsigned char* lds, const Gemm g, const Sched& S, const Epi& E) {
;     ...
;         const bool has_next = S.next(ui + 1, nxt);
;         const char* nA = has_next ? (const char*)S.opA(g, nxt) + (size_t)nxt.pm * tstepA : cA; const char* nB = has_next ? (const char*)S.opB(g, nxt) + (size_t)nxt.pn * tstepB : cB;
.LBB0_324:
	ds_read_b128 v[136:139], v132
	ds_read_b128 v[140:143], v132 offset:1024
	ds_read_b128 v[144:147], v132 offset:2048
	ds_read_b128 v[148:151], v132 offset:3072
	ds_read_b128 v[152:155], v133
	ds_read_b128 v[156:159], v133 offset:1024
	ds_read_b128 v[160:163], v133 offset:2048
	ds_read_b128 v[174:177], v133 offset:3072
	s_add_u32 s15, s10, 0xfff7c080
	s_addc_u32 s50, s11, -1
	s_cmp_eq_u32 s14, 28
	s_cselect_b32 s51, s25, s50
	s_cselect_b32 s50, s24, s15
	s_cselect_b32 s53, s3, s13
	s_cselect_b32 s52, s4, s12
	s_mov_b32 m0, s5
	v_lshl_add_u64 v[194:195], s[10:11], 0, v[172:173]
	ds_read_b128 v[178:181], v200
	ds_read_b128 v[182:185], v200 offset:1024
	ds_read_b128 v[186:189], v200 offset:2048
	ds_read_b128 v[190:193], v200 offset:3072
	ds_read_b128 v[202:205], v200 offset:4096
	ds_read_b128 v[206:209], v200 offset:5120
	ds_read_b128 v[216:219], v200 offset:6144
	ds_read_b128 v[220:223], v200 offset:7168
	global_load_lds_dwordx4 v[194:195], off
	v_lshl_add_u64 v[194:195], v[194:195], 0, s[96:97]
	s_mov_b32 m0, s23
	s_nop 0
	global_load_lds_dwordx4 v[194:195], off
	s_waitcnt vmcnt(8)
	s_waitcnt lgkmcnt(0)
	s_barrier
	s_waitcnt lgkmcnt(0)
	v_mfma_f32_16x16x32_bf16 v[120:123], v[136:139], v[178:181], v[120:123]
	v_mfma_f32_16x16x32_bf16 v[120:123], v[140:143], v[182:185], v[120:123]
	v_mfma_f32_16x16x32_bf16 v[116:119], v[144:147], v[178:181], v[116:119]
	v_mfma_f32_16x16x32_bf16 v[116:119], v[148:151], v[182:185], v[116:119]
	v_mfma_f32_16x16x32_bf16 v[104:107], v[136:139], v[186:189], v[104:107]
	v_mfma_f32_16x16x32_bf16 v[104:107], v[140:143], v[190:193], v[104:107]
	v_mfma_f32_16x16x32_bf16 v[100:103], v[144:147], v[186:189], v[100:103]
	v_mfma_f32_16x16x32_bf16 v[100:103], v[148:151], v[190:193], v[100:103]
	v_mfma_f32_16x16x32_bf16 v[88:91], v[136:139], v[202:205], v[88:91]
	v_mfma_f32_16x16x32_bf16 v[88:91], v[140:143], v[206:209], v[88:91]
	v_mfma_f32_16x16x32_bf16 v[84:87], v[144:147], v[202:205], v[84:87]
	v_mfma_f32_16x16x32_bf16 v[84:87], v[148:151], v[206:209], v[84:87]
	v_mfma_f32_16x16x32_bf16 v[72:75], v[136:139], v[216:219], v[72:75]
	v_mfma_f32_16x16x32_bf16 v[72:75], v[140:143], v[220:223], v[72:75]
	v_mfma_f32_16x16x32_bf16 v[68:71], v[144:147], v[216:219], v[68:71]
	v_mfma_f32_16x16x32_bf16 v[68:71], v[148:151], v[220:223], v[68:71]
	v_mfma_f32_16x16x32_bf16 v[128:131], v[152:155], v[178:181], v[128:131]
	v_mfma_f32_16x16x32_bf16 v[128:131], v[156:159], v[182:185], v[128:131]
	v_mfma_f32_16x16x32_bf16 v[124:127], v[160:163], v[178:181], v[124:127]
	v_mfma_f32_16x16x32_bf16 v[124:127], v[174:177], v[182:185], v[124:127]
	v_mfma_f32_16x16x32_bf16 v[112:115], v[152:155], v[186:189], v[112:115]
	v_mfma_f32_16x16x32_bf16 v[112:115], v[156:159], v[190:193], v[112:115]
	v_mfma_f32_16x16x32_bf16 v[108:111], v[160:163], v[186:189], v[108:111]
	v_mfma_f32_16x16x32_bf16 v[108:111], v[174:177], v[190:193], v[108:111]
	v_mfma_f32_16x16x32_bf16 v[96:99], v[152:155], v[202:205], v[96:99]
	v_mfma_f32_16x16x32_bf16 v[96:99], v[156:159], v[206:209], v[96:99]
	v_mfma_f32_16x16x32_bf16 v[92:95], v[160:163], v[202:205], v[92:95]
	v_mfma_f32_16x16x32_bf16 v[92:95], v[174:177], v[206:209], v[92:95]
	v_mfma_f32_16x16x32_bf16 v[80:83], v[152:155], v[216:219], v[80:83]
	v_mfma_f32_16x16x32_bf16 v[80:83], v[156:159], v[220:223], v[80:83]
	v_mfma_f32_16x16x32_bf16 v[76:79], v[160:163], v[216:219], v[76:79]
	v_mfma_f32_16x16x32_bf16 v[76:79], v[174:177], v[220:223], v[76:79]
	s_barrier
	s_mov_b32 m0, s28
	v_lshl_add_u64 v[194:195], s[52:53], 0, v[164:165]
	ds_read_b128 v[178:181], v200 offset:16384
	ds_read_b128 v[182:185], v200 offset:17408
	ds_read_b128 v[186:189], v200 offset:18432
	ds_read_b128 v[190:193], v200 offset:19456
	ds_read_b128 v[202:205], v200 offset:20480
	ds_read_b128 v[206:209], v200 offset:21504
	ds_read_b128 v[216:219], v200 offset:22528
	ds_read_b128 v[220:223], v200 offset:23552
	global_load_lds_dwordx4 v[194:195], off
	v_lshl_add_u64 v[214:215], v[194:195], 0, s[90:91]
	s_mov_b32 m0, s29
	s_nop 0
	global_load_lds_dwordx4 v[214:215], off
	v_lshl_add_u64 v[214:215], v[194:195], 0, s[54:55]
	s_mov_b32 m0, s33
	s_nop 0
	global_load_lds_dwordx4 v[214:215], off
	v_lshl_add_u64 v[214:215], v[194:195], 0, s[60:61]
	s_mov_b32 m0, s45
	s_nop 0
	global_load_lds_dwordx4 v[214:215], off
	v_lshl_add_u64 v[214:215], s[50:51], 0, v[166:167]
	s_mov_b32 m0, s30
	v_lshl_add_u64 v[224:225], v[214:215], 0, s[96:97]
	global_load_lds_dwordx4 v[214:215], off
	s_mov_b32 m0, s31
	s_nop 0
	global_load_lds_dwordx4 v[224:225], off
	s_waitcnt vmcnt(8)
	s_waitcnt lgkmcnt(0)
	s_barrier
	s_waitcnt lgkmcnt(0)
	v_mfma_f32_16x16x32_bf16 v[56:59], v[136:139], v[178:181], v[56:59]
	v_mfma_f32_16x16x32_bf16 v[56:59], v[140:143], v[182:185], v[56:59]
	v_mfma_f32_16x16x32_bf16 v[52:55], v[144:147], v[178:181], v[52:55]
	v_mfma_f32_16x16x32_bf16 v[52:55], v[148:151], v[182:185], v[52:55]
	v_mfma_f32_16x16x32_bf16 v[40:43], v[136:139], v[186:189], v[40:43]
	v_mfma_f32_16x16x32_bf16 v[40:43], v[140:143], v[190:193], v[40:43]
	v_mfma_f32_16x16x32_bf16 v[36:39], v[144:147], v[186:189], v[36:39]
	v_mfma_f32_16x16x32_bf16 v[36:39], v[148:151], v[190:193], v[36:39]
	v_mfma_f32_16x16x32_bf16 v[24:27], v[136:139], v[202:205], v[24:27]
	v_mfma_f32_16x16x32_bf16 v[24:27], v[140:143], v[206:209], v[24:27]
	v_mfma_f32_16x16x32_bf16 v[20:23], v[144:147], v[202:205], v[20:23]
	v_mfma_f32_16x16x32_bf16 v[20:23], v[148:151], v[206:209], v[20:23]
	v_mfma_f32_16x16x32_bf16 v[8:11], v[136:139], v[216:219], v[8:11]
	v_mfma_f32_16x16x32_bf16 v[8:11], v[140:143], v[220:223], v[8:11]
	v_mfma_f32_16x16x32_bf16 v[4:7], v[144:147], v[216:219], v[4:7]
	v_mfma_f32_16x16x32_bf16 v[4:7], v[148:151], v[220:223], v[4:7]
	v_mfma_f32_16x16x32_bf16 v[64:67], v[152:155], v[178:181], v[64:67]
	v_mfma_f32_16x16x32_bf16 v[64:67], v[156:159], v[182:185], v[64:67]
	v_mfma_f32_16x16x32_bf16 v[60:63], v[160:163], v[178:181], v[60:63]
	v_mfma_f32_16x16x32_bf16 v[60:63], v[174:177], v[182:185], v[60:63]
	v_mfma_f32_16x16x32_bf16 v[48:51], v[152:155], v[186:189], v[48:51]
	v_mfma_f32_16x16x32_bf16 v[48:51], v[156:159], v[190:193], v[48:51]
	v_mfma_f32_16x16x32_bf16 v[44:47], v[160:163], v[186:189], v[44:47]
	v_mfma_f32_16x16x32_bf16 v[44:47], v[174:177], v[190:193], v[44:47]
	v_mfma_f32_16x16x32_bf16 v[32:35], v[152:155], v[202:205], v[32:35]
	v_mfma_f32_16x16x32_bf16 v[32:35], v[156:159], v[206:209], v[32:35]
	v_mfma_f32_16x16x32_bf16 v[28:31], v[160:163], v[202:205], v[28:31]
	v_mfma_f32_16x16x32_bf16 v[28:31], v[174:177], v[206:209], v[28:31]
	v_mfma_f32_16x16x32_bf16 v[16:19], v[152:155], v[216:219], v[16:19]
	v_mfma_f32_16x16x32_bf16 v[16:19], v[156:159], v[220:223], v[16:19]
	v_mfma_f32_16x16x32_bf16 v[12:15], v[160:163], v[216:219], v[12:15]
	v_mfma_f32_16x16x32_bf16 v[12:15], v[174:177], v[220:223], v[12:15]
	s_barrier
	ds_read_b128 v[136:139], v134
	ds_read_b128 v[140:143], v134 offset:1024
	ds_read_b128 v[144:147], v134 offset:2048
	ds_read_b128 v[148:151], v134 offset:3072
	ds_read_b128 v[152:155], v135
	ds_read_b128 v[156:159], v135 offset:1024
	ds_read_b128 v[160:163], v135 offset:2048
	ds_read_b128 v[174:177], v135 offset:3072
	s_mov_b32 m0, s34
	v_lshl_add_u64 v[224:225], v[214:215], 0, s[82:83]
	ds_read_b128 v[178:181], v200 offset:32768
	ds_read_b128 v[182:185], v200 offset:33792
	ds_read_b128 v[186:189], v200 offset:34816
	ds_read_b128 v[190:193], v200 offset:35840
	ds_read_b128 v[202:205], v200 offset:36864
	ds_read_b128 v[206:209], v200 offset:37888
	ds_read_b128 v[216:219], v200 offset:38912
	ds_read_b128 v[220:223], v200 offset:39936
	global_load_lds_dwordx4 v[224:225], off
	v_lshl_add_u64 v[224:225], v[214:215], 0, s[64:65]
	s_mov_b32 m0, s35
	s_nop 0
	global_load_lds_dwordx4 v[224:225], off
	s_waitcnt vmcnt(8)
	s_waitcnt lgkmcnt(0)
	s_barrier
	s_waitcnt lgkmcnt(0)
	v_mfma_f32_16x16x32_bf16 v[120:123], v[136:139], v[178:181], v[120:123]
	v_mfma_f32_16x16x32_bf16 v[120:123], v[140:143], v[182:185], v[120:123]
	v_mfma_f32_16x16x32_bf16 v[116:119], v[144:147], v[178:181], v[116:119]
	v_mfma_f32_16x16x32_bf16 v[116:119], v[148:151], v[182:185], v[116:119]
	v_mfma_f32_16x16x32_bf16 v[104:107], v[136:139], v[186:189], v[104:107]
	v_mfma_f32_16x16x32_bf16 v[104:107], v[140:143], v[190:193], v[104:107]
	v_mfma_f32_16x16x32_bf16 v[100:103], v[144:147], v[186:189], v[100:103]
	v_mfma_f32_16x16x32_bf16 v[100:103], v[148:151], v[190:193], v[100:103]
	v_mfma_f32_16x16x32_bf16 v[88:91], v[136:139], v[202:205], v[88:91]
	v_mfma_f32_16x16x32_bf16 v[88:91], v[140:143], v[206:209], v[88:91]
	v_mfma_f32_16x16x32_bf16 v[84:87], v[144:147], v[202:205], v[84:87]
	v_mfma_f32_16x16x32_bf16 v[84:87], v[148:151], v[206:209], v[84:87]
	v_mfma_f32_16x16x32_bf16 v[72:75], v[136:139], v[216:219], v[72:75]
	v_mfma_f32_16x16x32_bf16 v[72:75], v[140:143], v[220:223], v[72:75]
	v_mfma_f32_16x16x32_bf16 v[68:71], v[144:147], v[216:219], v[68:71]
	v_mfma_f32_16x16x32_bf16 v[68:71], v[148:151], v[220:223], v[68:71]
	v_mfma_f32_16x16x32_bf16 v[128:131], v[152:155], v[178:181], v[128:131]
	v_mfma_f32_16x16x32_bf16 v[128:131], v[156:159], v[182:185], v[128:131]
	v_mfma_f32_16x16x32_bf16 v[124:127], v[160:163], v[178:181], v[124:127]
	v_mfma_f32_16x16x32_bf16 v[124:127], v[174:177], v[182:185], v[124:127]
	v_mfma_f32_16x16x32_bf16 v[112:115], v[152:155], v[186:189], v[112:115]
	v_mfma_f32_16x16x32_bf16 v[112:115], v[156:159], v[190:193], v[112:115]
	v_mfma_f32_16x16x32_bf16 v[108:111], v[160:163], v[186:189], v[108:111]
	v_mfma_f32_16x16x32_bf16 v[108:111], v[174:177], v[190:193], v[108:111]
	v_mfma_f32_16x16x32_bf16 v[96:99], v[152:155], v[202:205], v[96:99]
	v_mfma_f32_16x16x32_bf16 v[96:99], v[156:159], v[206:209], v[96:99]
	v_mfma_f32_16x16x32_bf16 v[92:95], v[160:163], v[202:205], v[92:95]
	v_mfma_f32_16x16x32_bf16 v[92:95], v[174:177], v[206:209], v[92:95]
	v_mfma_f32_16x16x32_bf16 v[80:83], v[152:155], v[216:219], v[80:83]
	v_mfma_f32_16x16x32_bf16 v[80:83], v[156:159], v[220:223], v[80:83]
	v_mfma_f32_16x16x32_bf16 v[76:79], v[160:163], v[216:219], v[76:79]
	v_mfma_f32_16x16x32_bf16 v[76:79], v[174:177], v[220:223], v[76:79]
	s_barrier
; #define PG8_MMA(ai, bj, At, Bt) do { __builtin_amdgcn_s_setprio(1); _Pragma("unroll") for (int m = 0; m < 4; ++m) _Pragma("unroll") for (int n = 0; n < 2; ++n) _Pragma("unroll") for (int k = 0; k < 2; ++k) \
;         acc[ai][bj][m][n] = __builtin_amdgcn_mfma_f32_16x16x32_bf16(Bt[n][k], At[m][k], acc[ai][bj][m][n], 0, 0, 0); __builtin_amdgcn_s_setprio(0); } while (0)
; #define PG8_WAIT_V(n) asm volatile("s_waitcnt vmcnt(" #n ")" ::: "memory")
; #define PG8_BAR __builtin_amdgcn_s_barrier()
; #define PG8_TRIP_HEAD(T) const int t = (T); const bool last = (t == nt - 2); \
;             const char* a1 = cA + (size_t)(t + 1) * kstep; \
;             const char* a2 = last ? nA : cA + (size_t)(t + 2) * kstep; const char* b2 = last ? nB : cB + (size_t)(t + 2) * kstep; \
;             const char* a3 = a2 + kstep; const char* b3 = b2 + kstep; \
;             if (last && has_next) S.a_ready(nxt);
; template <class Epi, class Sched, bool ALIGN_EPI = false, bool SP2 = false>
; __device__ __forceinline__ void gemm_phase(PG8_LAS unsigned char* lds, const Gemm g, const Sched& S, const Epi& E) {
;     ...
;         if constexpr (SP2) {
;             { PG8_TRIP_HEAD(0) PG8_TRIP_SP2(asm volatile("s_waitcnt vmcnt(%0)" :: "n"(8 + Epi::NST) : "memory"), PG8_MMAZ) }
;             for (int tt = 2; tt < nt; tt += 2) { PG8_TRIP_HEAD(tt) PG8_TRIP_SP2(PG8_WAIT_V(8), PG8_MMA) }
;     ...
;         if constexpr (ALIGN_EPI) { if (wr == 0) PG8_BAR; }
	s_mov_b32 m0, s46
	v_lshl_add_u64 v[224:225], v[194:195], 0, s[78:79]
	ds_read_b128 v[178:181], v200 offset:49152
	ds_read_b128 v[182:185], v200 offset:50176
	ds_read_b128 v[186:189], v200 offset:51200
	ds_read_b128 v[190:193], v200 offset:52224
	ds_read_b128 v[202:205], v200 offset:53248
	ds_read_b128 v[206:209], v200 offset:54272
	ds_read_b128 v[216:219], v200 offset:55296
	ds_read_b128 v[220:223], v200 offset:56320
	global_load_lds_dwordx4 v[224:225], off
	v_lshl_add_u64 v[224:225], v[194:195], 0, s[84:85]
	s_mov_b32 m0, s47
	s_nop 0
	global_load_lds_dwordx4 v[224:225], off
	v_lshl_add_u64 v[224:225], v[194:195], 0, s[56:57]
	s_mov_b32 m0, s48
	v_lshl_add_u64 v[194:195], v[194:195], 0, s[62:63]
	global_load_lds_dwordx4 v[224:225], off
	s_mov_b32 m0, s49
	s_nop 0
	global_load_lds_dwordx4 v[194:195], off
	v_lshl_add_u64 v[194:195], v[214:215], 0, s[78:79]
	s_mov_b32 m0, s38
	s_nop 0
	global_load_lds_dwordx4 v[194:195], off
	v_lshl_add_u64 v[194:195], v[214:215], 0, s[92:93]
	s_mov_b32 m0, s39
	s_nop 0
	global_load_lds_dwordx4 v[194:195], off
	s_waitcnt vmcnt(8)
	s_waitcnt lgkmcnt(0)
	s_barrier
	s_waitcnt lgkmcnt(0)
	v_mfma_f32_16x16x32_bf16 v[56:59], v[136:139], v[178:181], v[56:59]
	v_mfma_f32_16x16x32_bf16 v[56:59], v[140:143], v[182:185], v[56:59]
	v_mfma_f32_16x16x32_bf16 v[52:55], v[144:147], v[178:181], v[52:55]
	v_mfma_f32_16x16x32_bf16 v[52:55], v[148:151], v[182:185], v[52:55]
	v_mfma_f32_16x16x32_bf16 v[40:43], v[136:139], v[186:189], v[40:43]
	v_mfma_f32_16x16x32_bf16 v[40:43], v[140:143], v[190:193], v[40:43]
	v_mfma_f32_16x16x32_bf16 v[36:39], v[144:147], v[186:189], v[36:39]
	v_mfma_f32_16x16x32_bf16 v[36:39], v[148:151], v[190:193], v[36:39]
	v_mfma_f32_16x16x32_bf16 v[24:27], v[136:139], v[202:205], v[24:27]
	v_mfma_f32_16x16x32_bf16 v[24:27], v[140:143], v[206:209], v[24:27]
	v_mfma_f32_16x16x32_bf16 v[20:23], v[144:147], v[202:205], v[20:23]
	v_mfma_f32_16x16x32_bf16 v[20:23], v[148:151], v[206:209], v[20:23]
	v_mfma_f32_16x16x32_bf16 v[8:11], v[136:139], v[216:219], v[8:11]
	v_mfma_f32_16x16x32_bf16 v[8:11], v[140:143], v[220:223], v[8:11]
	v_mfma_f32_16x16x32_bf16 v[4:7], v[144:147], v[216:219], v[4:7]
	v_mfma_f32_16x16x32_bf16 v[4:7], v[148:151], v[220:223], v[4:7]
	v_mfma_f32_16x16x32_bf16 v[64:67], v[152:155], v[178:181], v[64:67]
	v_mfma_f32_16x16x32_bf16 v[64:67], v[156:159], v[182:185], v[64:67]
	v_mfma_f32_16x16x32_bf16 v[60:63], v[160:163], v[178:181], v[60:63]
	v_mfma_f32_16x16x32_bf16 v[60:63], v[174:177], v[182:185], v[60:63]
	v_mfma_f32_16x16x32_bf16 v[48:51], v[152:155], v[186:189], v[48:51]
	v_mfma_f32_16x16x32_bf16 v[48:51], v[156:159], v[190:193], v[48:51]
	v_mfma_f32_16x16x32_bf16 v[44:47], v[160:163], v[186:189], v[44:47]
	v_mfma_f32_16x16x32_bf16 v[44:47], v[174:177], v[190:193], v[44:47]
	v_mfma_f32_16x16x32_bf16 v[32:35], v[152:155], v[202:205], v[32:35]
	v_mfma_f32_16x16x32_bf16 v[32:35], v[156:159], v[206:209], v[32:35]
	v_mfma_f32_16x16x32_bf16 v[28:31], v[160:163], v[202:205], v[28:31]
	v_mfma_f32_16x16x32_bf16 v[28:31], v[174:177], v[206:209], v[28:31]
	v_mfma_f32_16x16x32_bf16 v[16:19], v[152:155], v[216:219], v[16:19]
	v_mfma_f32_16x16x32_bf16 v[16:19], v[156:159], v[220:223], v[16:19]
	v_mfma_f32_16x16x32_bf16 v[12:15], v[160:163], v[216:219], v[12:15]
	v_mfma_f32_16x16x32_bf16 v[12:15], v[174:177], v[220:223], v[12:15]
	s_barrier
	s_add_i32 s14, s14, 2
	s_add_u32 s10, s10, 0x100
	s_addc_u32 s11, s11, 0
	s_add_u32 s12, s12, 0x100
	s_addc_u32 s13, s13, 0
	s_cmp_gt_u32 s14, 29
	s_cbranch_scc0 .LBB0_324
	s_and_b64 vcc, exec, s[18:19]
	s_cbranch_vccz .LBB0_327
	s_barrier

;     __device__ bool next(int i, Unit& u) const { const int rounds = nwg / G; if (i >= rounds) return false; return StaticOrder::next(rounds - 1 - i, u); }
;     __device__ bool next(int i, Unit& u) const { const int rounds = nwg / G; if (i >= 2 * rounds) return false; const bool ok = StaticOrder::next(i >= rounds ? i - rounds : i, u); u.z = (i >= rounds) ? 1 : 0; return ok; }
; #define PG8_TRIP_HEAD(T) const int t = (T); const bool last = (t == nt - 2); \
;             const char* a1 = cA + (size_t)(t + 1) * kstep; \
;             const char* a2 = last ? nA : cA + (size_t)(t + 2) * kstep; const char* b2 = last ? nB : cB + (size_t)(t + 2) * kstep; \
;             const char* a3 = a2 + kstep; const char* b3 = b2 + kstep; \
;             if (last && has_next) S.a_ready(nxt);
; template <class Epi, class Sched, bool ALIGN_EPI = false, bool SP2 = false>
; __device__ __forceinline__ void gemm_phase(PG8_LAS unsigned char* lds, const Gemm g, const Sched& S, const Epi& E) {
;     ...
;         const bool has_next = S.next(ui + 1, nxt);
;         const char* nA = has_next ? (const char*)S.opA(g, nxt) + (size_t)nxt.pm * tstepA : cA; const char* nB = has_next ? (const char*)S.opB(g, nxt) + (size_t)nxt.pn * tstepB : cB;
;     ...
;         if constexpr (SP2) {
;             { PG8_TRIP_HEAD(0) PG8_TRIP_SP2(asm volatile("s_waitcnt vmcnt(%0)" :: "n"(8 + Epi::NST) : "memory"), PG8_MMAZ) }
.LBB0_593:
	v_readlane_b32 s18, v253, 7
	v_readlane_b32 s34, v254, 59
	s_cmp_eq_u32 s29, 0
	v_readlane_b32 s19, v253, 8
	v_readlane_b32 s35, v254, 60
	s_cselect_b32 s33, s35, s19
	s_cselect_b32 s34, s34, s18
	s_ashr_i32 s15, s14, 31
	s_lshl_b64 s[18:19], s[14:15], 20
	s_add_u32 s18, s34, s18
	s_addc_u32 s19, s33, s19
	s_and_b64 s[4:5], s[4:5], exec
	s_cselect_b32 s4, s19, s9
	s_cselect_b32 s5, s18, s8
	s_add_i32 s35, 0, 0x10000
	s_add_i32 s37, 0, 0x14000
	v_add_u32_e32 v116, s35, v219
	v_add_u32_e32 v117, s37, v219
	ds_read_b128 v[4:7], v116
	ds_read_b128 v[8:11], v116 offset:1024
	ds_read_b128 v[12:15], v116 offset:2048
	ds_read_b128 v[16:19], v116 offset:3072
	ds_read_b128 v[20:23], v117
	ds_read_b128 v[24:27], v117 offset:1024
	ds_read_b128 v[28:31], v117 offset:2048
	ds_read_b128 v[32:35], v117 offset:3072
	s_mov_b32 s15, 0
	v_lshl_add_u64 v[192:193], s[20:21], 0, v[196:197]
	s_mov_b64 s[38:39], 0x84080
	s_add_i32 s33, s23, 0xc000
	v_lshl_add_u64 v[68:69], v[192:193], 0, s[38:39]
	s_mov_b32 m0, s33
	s_mov_b64 s[38:39], 0xc6080
	s_add_i32 s34, s23, 0xe000
	ds_read_b128 v[36:39], v221
	ds_read_b128 v[40:43], v221 offset:1024
	ds_read_b128 v[44:47], v221 offset:2048
	ds_read_b128 v[48:51], v221 offset:3072
	ds_read_b128 v[52:55], v221 offset:4096
	ds_read_b128 v[56:59], v221 offset:5120
	ds_read_b128 v[60:63], v221 offset:6144
	ds_read_b128 v[64:67], v221 offset:7168
	global_load_lds_dwordx4 v[68:69], off
	v_lshl_add_u64 v[68:69], v[192:193], 0, s[38:39]
	s_mov_b32 m0, s34
	s_nop 0
	global_load_lds_dwordx4 v[68:69], off
	s_waitcnt vmcnt(8)
	s_waitcnt lgkmcnt(0)
	s_barrier
	s_waitcnt lgkmcnt(0)
	v_mfma_f32_16x16x32_bf16 v[92:95], v[4:7], v[60:63], 0
	v_mfma_f32_16x16x32_bf16 v[68:71], v[4:7], v[36:39], 0
	v_mfma_f32_16x16x32_bf16 v[72:75], v[12:15], v[36:39], 0
	v_mfma_f32_16x16x32_bf16 v[76:79], v[4:7], v[44:47], 0
	v_mfma_f32_16x16x32_bf16 v[80:83], v[12:15], v[44:47], 0
	v_mfma_f32_16x16x32_bf16 v[84:87], v[4:7], v[52:55], 0
	v_mfma_f32_16x16x32_bf16 v[88:91], v[12:15], v[52:55], 0
	v_mfma_f32_16x16x32_bf16 v[100:103], v[8:11], v[64:67], v[92:95]
	v_mfma_f32_16x16x32_bf16 v[92:95], v[12:15], v[60:63], 0
	v_mfma_f32_16x16x32_bf16 v[68:71], v[8:11], v[40:43], v[68:71]
	v_mfma_f32_16x16x32_bf16 v[72:75], v[16:19], v[40:43], v[72:75]
	v_mfma_f32_16x16x32_bf16 v[76:79], v[8:11], v[48:51], v[76:79]
	v_mfma_f32_16x16x32_bf16 v[80:83], v[16:19], v[48:51], v[80:83]
	v_mfma_f32_16x16x32_bf16 v[84:87], v[8:11], v[56:59], v[84:87]
	v_mfma_f32_16x16x32_bf16 v[88:91], v[16:19], v[56:59], v[88:91]
	v_mfma_f32_16x16x32_bf16 v[104:107], v[16:19], v[64:67], v[92:95]
	v_mfma_f32_16x16x32_bf16 v[92:95], v[20:23], v[36:39], 0
	v_mfma_f32_16x16x32_bf16 v[36:39], v[28:31], v[36:39], 0
	v_mfma_f32_16x16x32_bf16 v[118:121], v[24:27], v[40:43], v[92:95]
	v_mfma_f32_16x16x32_bf16 v[36:39], v[32:35], v[40:43], v[36:39]
	v_mfma_f32_16x16x32_bf16 v[40:43], v[20:23], v[44:47], 0
	v_mfma_f32_16x16x32_bf16 v[44:47], v[28:31], v[44:47], 0
	v_mfma_f32_16x16x32_bf16 v[40:43], v[24:27], v[48:51], v[40:43]
	v_mfma_f32_16x16x32_bf16 v[44:47], v[32:35], v[48:51], v[44:47]
	v_mfma_f32_16x16x32_bf16 v[48:51], v[20:23], v[52:55], 0
	v_mfma_f32_16x16x32_bf16 v[52:55], v[28:31], v[52:55], 0
	v_mfma_f32_16x16x32_bf16 v[48:51], v[24:27], v[56:59], v[48:51]
	v_mfma_f32_16x16x32_bf16 v[52:55], v[32:35], v[56:59], v[52:55]
	v_mfma_f32_16x16x32_bf16 v[56:59], v[20:23], v[60:63], 0
	v_mfma_f32_16x16x32_bf16 v[60:63], v[28:31], v[60:63], 0
	v_mfma_f32_16x16x32_bf16 v[56:59], v[24:27], v[64:67], v[56:59]
	v_mfma_f32_16x16x32_bf16 v[60:63], v[32:35], v[64:67], v[60:63]
	s_barrier
	v_lshl_add_u64 v[250:251], s[8:9], 0, v[194:195]
	s_mov_b64 s[40:41], 0x100
	s_add_i32 s35, s35, s22
	v_lshl_add_u64 v[134:135], v[250:251], 0, s[40:41]
	s_mov_b32 m0, s35
	s_mov_b64 s[38:39], 0x40100
	s_add_i32 s36, s35, 0x2000
	ds_read_b128 v[64:67], v221 offset:16384
	ds_read_b128 v[92:95], v221 offset:17408
	ds_read_b128 v[96:99], v221 offset:18432
	ds_read_b128 v[108:111], v221 offset:19456
	ds_read_b128 v[112:115], v221 offset:20480
	ds_read_b128 v[122:125], v221 offset:21504
	ds_read_b128 v[126:129], v221 offset:22528
	ds_read_b128 v[130:133], v221 offset:23552
	global_load_lds_dwordx4 v[134:135], off
	v_lshl_add_u64 v[134:135], v[250:251], 0, s[38:39]
	s_mov_b32 m0, s36
	s_mov_b64 s[38:39], 0x80100
	s_add_i32 s37, s37, s22
	global_load_lds_dwordx4 v[134:135], off
	v_lshl_add_u64 v[134:135], v[250:251], 0, s[38:39]
	s_mov_b32 m0, s37
	s_mov_b64 s[38:39], 0xc0100
	global_load_lds_dwordx4 v[134:135], off
	v_lshl_add_u64 v[134:135], v[250:251], 0, s[38:39]
	s_add_i32 s38, s37, 0x2000
	s_mov_b32 m0, s38
	s_nop 0
	global_load_lds_dwordx4 v[134:135], off
	v_lshl_add_u64 v[134:135], v[192:193], 0, s[40:41]
	s_mov_b32 m0, s23
	s_mov_b64 s[40:41], 0x42100
	global_load_lds_dwordx4 v[134:135], off
	v_lshl_add_u64 v[134:135], v[192:193], 0, s[40:41]
	s_mov_b32 m0, s24
	s_nop 0
	global_load_lds_dwordx4 v[134:135], off
	s_waitcnt vmcnt(8)
	s_waitcnt lgkmcnt(0)
	s_barrier
; #define PG8_TRIP_HEAD(T) const int t = (T); const bool last = (t == nt - 2); \
;             const char* a1 = cA + (size_t)(t + 1) * kstep; \
;             const char* a2 = last ? nA : cA + (size_t)(t + 2) * kstep; const char* b2 = last ? nB : cB + (size_t)(t + 2) * kstep; \
;             const char* a3 = a2 + kstep; const char* b3 = b2 + kstep; \
;             if (last && has_next) S.a_ready(nxt);
; template <class Epi, class Sched, bool ALIGN_EPI = false, bool SP2 = false>
; __device__ __forceinline__ void gemm_phase(PG8_LAS unsigned char* lds, const Gemm g, const Sched& S, const Epi& E) {
;     ...
;         if constexpr (SP2) {
;             { PG8_TRIP_HEAD(0) PG8_TRIP_SP2(asm volatile("s_waitcnt vmcnt(%0)" :: "n"(8 + Epi::NST) : "memory"), PG8_MMAZ) }
	s_waitcnt lgkmcnt(0)
	v_mfma_f32_16x16x32_bf16 v[134:137], v[4:7], v[64:67], 0
	v_mfma_f32_16x16x32_bf16 v[144:147], v[4:7], v[96:99], 0
	v_mfma_f32_16x16x32_bf16 v[152:155], v[4:7], v[112:115], 0
	v_mfma_f32_16x16x32_bf16 v[4:7], v[4:7], v[126:129], 0
	v_mfma_f32_16x16x32_bf16 v[136:139], v[8:11], v[92:95], v[134:137]
	v_mfma_f32_16x16x32_bf16 v[144:147], v[8:11], v[108:111], v[144:147]
	v_mfma_f32_16x16x32_bf16 v[152:155], v[8:11], v[122:125], v[152:155]
	v_mfma_f32_16x16x32_bf16 v[4:7], v[8:11], v[130:133], v[4:7]
	v_mfma_f32_16x16x32_bf16 v[8:11], v[12:15], v[126:129], 0
	v_mfma_f32_16x16x32_bf16 v[140:143], v[12:15], v[64:67], 0
	v_mfma_f32_16x16x32_bf16 v[148:151], v[12:15], v[96:99], 0
	v_mfma_f32_16x16x32_bf16 v[156:159], v[12:15], v[112:115], 0
	v_mfma_f32_16x16x32_bf16 v[8:11], v[16:19], v[130:133], v[8:11]
	v_mfma_f32_16x16x32_bf16 v[140:143], v[16:19], v[92:95], v[140:143]
	v_mfma_f32_16x16x32_bf16 v[148:151], v[16:19], v[108:111], v[148:151]
	v_mfma_f32_16x16x32_bf16 v[156:159], v[16:19], v[122:125], v[156:159]
	v_mfma_f32_16x16x32_bf16 v[12:15], v[20:23], v[64:67], 0
	v_mfma_f32_16x16x32_bf16 v[160:163], v[24:27], v[92:95], v[12:15]
	v_mfma_f32_16x16x32_bf16 v[12:15], v[28:31], v[64:67], 0
	v_mfma_f32_16x16x32_bf16 v[164:167], v[32:35], v[92:95], v[12:15]
	v_mfma_f32_16x16x32_bf16 v[12:15], v[20:23], v[96:99], 0
	v_mfma_f32_16x16x32_bf16 v[168:171], v[24:27], v[108:111], v[12:15]
	v_mfma_f32_16x16x32_bf16 v[12:15], v[28:31], v[96:99], 0
	v_mfma_f32_16x16x32_bf16 v[172:175], v[32:35], v[108:111], v[12:15]
	v_mfma_f32_16x16x32_bf16 v[12:15], v[20:23], v[112:115], 0
	v_mfma_f32_16x16x32_bf16 v[176:179], v[24:27], v[122:125], v[12:15]
	v_mfma_f32_16x16x32_bf16 v[12:15], v[28:31], v[112:115], 0
	v_mfma_f32_16x16x32_bf16 v[180:183], v[32:35], v[122:125], v[12:15]
	v_mfma_f32_16x16x32_bf16 v[12:15], v[20:23], v[126:129], 0
	v_mfma_f32_16x16x32_bf16 v[184:187], v[24:27], v[130:133], v[12:15]
	v_mfma_f32_16x16x32_bf16 v[12:15], v[28:31], v[126:129], 0
	v_mfma_f32_16x16x32_bf16 v[188:191], v[32:35], v[130:133], v[12:15]
	s_barrier
	s_add_i32 s39, 0, 0x18000
	s_add_i32 s41, 0, 0x1c000
	v_add_u32_e32 v134, s39, v219
	v_add_u32_e32 v135, s41, v219
	s_nop 0
	ds_read_b128 v[12:15], v134
	ds_read_b128 v[16:19], v134 offset:1024
	ds_read_b128 v[20:23], v134 offset:2048
	ds_read_b128 v[24:27], v134 offset:3072
	ds_read_b128 v[202:205], v135
	ds_read_b128 v[206:209], v135 offset:1024
	ds_read_b128 v[222:225], v135 offset:2048
	ds_read_b128 v[226:229], v135 offset:3072
	s_mov_b64 s[42:43], 0x84100
	s_mov_b32 m0, s25
	v_lshl_add_u64 v[92:93], v[192:193], 0, s[42:43]
	s_mov_b64 s[42:43], 0xc6100
	ds_read_b128 v[28:31], v221 offset:32768
	ds_read_b128 v[32:35], v221 offset:33792
	ds_read_b128 v[64:67], v221 offset:34816
	ds_read_b128 v[230:233], v221 offset:35840
	ds_read_b128 v[234:237], v221 offset:36864
	ds_read_b128 v[238:241], v221 offset:37888
	ds_read_b128 v[242:245], v221 offset:38912
	ds_read_b128 v[246:249], v221 offset:39936
	global_load_lds_dwordx4 v[92:93], off
	v_lshl_add_u64 v[92:93], v[192:193], 0, s[42:43]
	s_mov_b32 m0, s26
	s_nop 0
	global_load_lds_dwordx4 v[92:93], off
	s_waitcnt vmcnt(8)
	s_waitcnt lgkmcnt(0)
	s_barrier
	s_waitcnt lgkmcnt(0)
	v_mfma_f32_16x16x32_bf16 v[68:71], v[12:15], v[28:31], v[68:71]
	v_mfma_f32_16x16x32_bf16 v[130:133], v[16:19], v[32:35], v[68:71]
	v_mfma_f32_16x16x32_bf16 v[68:71], v[20:23], v[28:31], v[72:75]
	v_mfma_f32_16x16x32_bf16 v[126:129], v[24:27], v[32:35], v[68:71]
	v_mfma_f32_16x16x32_bf16 v[68:71], v[12:15], v[64:67], v[76:79]
	v_mfma_f32_16x16x32_bf16 v[112:115], v[16:19], v[230:233], v[68:71]
	v_mfma_f32_16x16x32_bf16 v[68:71], v[20:23], v[64:67], v[80:83]
	v_mfma_f32_16x16x32_bf16 v[108:111], v[24:27], v[230:233], v[68:71]
	v_mfma_f32_16x16x32_bf16 v[68:71], v[12:15], v[234:237], v[84:87]
	v_mfma_f32_16x16x32_bf16 v[96:99], v[16:19], v[238:241], v[68:71]
	v_mfma_f32_16x16x32_bf16 v[68:71], v[20:23], v[234:237], v[88:91]
	v_mfma_f32_16x16x32_bf16 v[92:95], v[24:27], v[238:241], v[68:71]
	v_mfma_f32_16x16x32_bf16 v[68:71], v[12:15], v[242:245], v[100:103]
	v_mfma_f32_16x16x32_bf16 v[80:83], v[16:19], v[246:249], v[68:71]
	v_mfma_f32_16x16x32_bf16 v[68:71], v[20:23], v[242:245], v[104:107]
	v_mfma_f32_16x16x32_bf16 v[76:79], v[24:27], v[246:249], v[68:71]
	v_mfma_f32_16x16x32_bf16 v[68:71], v[202:205], v[28:31], v[118:121]
	v_mfma_f32_16x16x32_bf16 v[28:31], v[222:225], v[28:31], v[36:39]
	v_mfma_f32_16x16x32_bf16 v[118:121], v[226:229], v[32:35], v[28:31]
	v_mfma_f32_16x16x32_bf16 v[28:31], v[202:205], v[64:67], v[40:43]
	v_mfma_f32_16x16x32_bf16 v[104:107], v[206:209], v[230:233], v[28:31]
	v_mfma_f32_16x16x32_bf16 v[28:31], v[222:225], v[64:67], v[44:47]
	v_mfma_f32_16x16x32_bf16 v[100:103], v[226:229], v[230:233], v[28:31]
	v_mfma_f32_16x16x32_bf16 v[28:31], v[202:205], v[234:237], v[48:51]
	v_mfma_f32_16x16x32_bf16 v[88:91], v[206:209], v[238:241], v[28:31]
	v_mfma_f32_16x16x32_bf16 v[28:31], v[222:225], v[234:237], v[52:55]
	v_mfma_f32_16x16x32_bf16 v[84:87], v[226:229], v[238:241], v[28:31]
	v_mfma_f32_16x16x32_bf16 v[28:31], v[202:205], v[242:245], v[56:59]
	v_mfma_f32_16x16x32_bf16 v[72:75], v[206:209], v[246:249], v[28:31]
	v_mfma_f32_16x16x32_bf16 v[28:31], v[222:225], v[242:245], v[60:63]
	v_mfma_f32_16x16x32_bf16 v[122:125], v[206:209], v[32:35], v[68:71]
	v_mfma_f32_16x16x32_bf16 v[68:71], v[226:229], v[246:249], v[28:31]
	s_barrier
; #define PG8_MMA(ai, bj, At, Bt) do { __builtin_amdgcn_s_setprio(1); _Pragma("unroll") for (int m = 0; m < 4; ++m) _Pragma("unroll") for (int n = 0; n < 2; ++n) _Pragma("unroll") for (int k = 0; k < 2; ++k) \
;         acc[ai][bj][m][n] = __builtin_amdgcn_mfma_f32_16x16x32_bf16(Bt[n][k], At[m][k], acc[ai][bj][m][n], 0, 0, 0); __builtin_amdgcn_s_setprio(0); } while (0)
; #define PG8_WAIT_V(n) asm volatile("s_waitcnt vmcnt(" #n ")" ::: "memory")
; #define PG8_TRIP_HEAD(T) const int t = (T); const bool last = (t == nt - 2); \
;             const char* a1 = cA + (size_t)(t + 1) * kstep; \
;             const char* a2 = last ? nA : cA + (size_t)(t + 2) * kstep; const char* b2 = last ? nB : cB + (size_t)(t + 2) * kstep; \
;             const char* a3 = a2 + kstep; const char* b3 = b2 + kstep; \
;             if (last && has_next) S.a_ready(nxt);
; template <class Epi, class Sched, bool ALIGN_EPI = false, bool SP2 = false>
; __device__ __forceinline__ void gemm_phase(PG8_LAS unsigned char* lds, const Gemm g, const Sched& S, const Epi& E) {
;     ...
;         if constexpr (SP2) {
;             { PG8_TRIP_HEAD(0) PG8_TRIP_SP2(asm volatile("s_waitcnt vmcnt(%0)" :: "n"(8 + Epi::NST) : "memory"), PG8_MMAZ) }
;             for (int tt = 2; tt < nt; tt += 2) { PG8_TRIP_HEAD(tt) PG8_TRIP_SP2(PG8_WAIT_V(8), PG8_MMA) }
	s_mov_b64 s[44:45], 0x180
	s_add_i32 s39, s39, s22
	s_nop 1
	v_lshl_add_u64 v[28:29], v[250:251], 0, s[44:45]
	s_mov_b32 m0, s39
	s_mov_b64 s[42:43], 0x40180
	s_add_i32 s40, s39, 0x2000
	ds_read_b128 v[36:39], v221 offset:49152
	ds_read_b128 v[40:43], v221 offset:50176
	ds_read_b128 v[230:233], v221 offset:51200
	ds_read_b128 v[234:237], v221 offset:52224
	ds_read_b128 v[238:241], v221 offset:53248
	ds_read_b128 v[242:245], v221 offset:54272
	ds_read_b128 v[246:249], v221 offset:55296
	ds_read_b128 v[214:217], v221 offset:56320
	global_load_lds_dwordx4 v[28:29], off
	v_lshl_add_u64 v[28:29], v[250:251], 0, s[42:43]
	s_mov_b32 m0, s40
	s_mov_b64 s[42:43], 0x80180
	s_add_i32 s41, s41, s22
	global_load_lds_dwordx4 v[28:29], off
	v_lshl_add_u64 v[28:29], v[250:251], 0, s[42:43]
	s_mov_b32 m0, s41
	s_mov_b64 s[42:43], 0xc0180
	global_load_lds_dwordx4 v[28:29], off
	v_lshl_add_u64 v[28:29], v[250:251], 0, s[42:43]
	s_add_i32 s42, s41, 0x2000
	s_mov_b32 m0, s42
	s_nop 0
	global_load_lds_dwordx4 v[28:29], off
	v_lshl_add_u64 v[28:29], v[192:193], 0, s[44:45]
	s_mov_b32 m0, s27
	s_mov_b64 s[44:45], 0x42180
	global_load_lds_dwordx4 v[28:29], off
	v_lshl_add_u64 v[28:29], v[192:193], 0, s[44:45]
	s_mov_b32 m0, s28
	s_nop 0
	global_load_lds_dwordx4 v[28:29], off
	s_waitcnt vmcnt(8)
	s_waitcnt lgkmcnt(0)
	s_barrier
	s_waitcnt lgkmcnt(0)
	v_mfma_f32_16x16x32_bf16 v[28:31], v[12:15], v[36:39], v[136:139]
	v_mfma_f32_16x16x32_bf16 v[64:67], v[16:19], v[40:43], v[28:31]
	v_mfma_f32_16x16x32_bf16 v[28:31], v[20:23], v[36:39], v[140:143]
	v_mfma_f32_16x16x32_bf16 v[60:63], v[24:27], v[40:43], v[28:31]
	v_mfma_f32_16x16x32_bf16 v[28:31], v[12:15], v[230:233], v[144:147]
	v_mfma_f32_16x16x32_bf16 v[48:51], v[16:19], v[234:237], v[28:31]
	v_mfma_f32_16x16x32_bf16 v[28:31], v[20:23], v[230:233], v[148:151]
	v_mfma_f32_16x16x32_bf16 v[44:47], v[24:27], v[234:237], v[28:31]
	v_mfma_f32_16x16x32_bf16 v[28:31], v[12:15], v[238:241], v[152:155]
	v_mfma_f32_16x16x32_bf16 v[4:7], v[12:15], v[246:249], v[4:7]
	v_mfma_f32_16x16x32_bf16 v[32:35], v[16:19], v[242:245], v[28:31]
	v_mfma_f32_16x16x32_bf16 v[28:31], v[20:23], v[238:241], v[156:159]
	v_mfma_f32_16x16x32_bf16 v[16:19], v[16:19], v[214:217], v[4:7]
	v_mfma_f32_16x16x32_bf16 v[4:7], v[20:23], v[246:249], v[8:11]
	v_mfma_f32_16x16x32_bf16 v[28:31], v[24:27], v[242:245], v[28:31]
	v_mfma_f32_16x16x32_bf16 v[12:15], v[24:27], v[214:217], v[4:7]
	v_mfma_f32_16x16x32_bf16 v[4:7], v[202:205], v[36:39], v[160:163]
	v_mfma_f32_16x16x32_bf16 v[56:59], v[206:209], v[40:43], v[4:7]
	v_mfma_f32_16x16x32_bf16 v[4:7], v[222:225], v[36:39], v[164:167]
	v_mfma_f32_16x16x32_bf16 v[52:55], v[226:229], v[40:43], v[4:7]
	v_mfma_f32_16x16x32_bf16 v[4:7], v[202:205], v[230:233], v[168:171]
	v_mfma_f32_16x16x32_bf16 v[40:43], v[206:209], v[234:237], v[4:7]
	v_mfma_f32_16x16x32_bf16 v[4:7], v[222:225], v[230:233], v[172:175]
	v_mfma_f32_16x16x32_bf16 v[36:39], v[226:229], v[234:237], v[4:7]
	v_mfma_f32_16x16x32_bf16 v[4:7], v[202:205], v[238:241], v[176:179]
	v_mfma_f32_16x16x32_bf16 v[24:27], v[206:209], v[242:245], v[4:7]
	v_mfma_f32_16x16x32_bf16 v[4:7], v[222:225], v[238:241], v[180:183]
	v_mfma_f32_16x16x32_bf16 v[20:23], v[226:229], v[242:245], v[4:7]
	v_mfma_f32_16x16x32_bf16 v[4:7], v[202:205], v[246:249], v[184:187]
	v_mfma_f32_16x16x32_bf16 v[8:11], v[206:209], v[214:217], v[4:7]
	v_mfma_f32_16x16x32_bf16 v[4:7], v[222:225], v[246:249], v[188:191]
	v_mfma_f32_16x16x32_bf16 v[4:7], v[226:229], v[214:217], v[4:7]
	s_barrier
	s_add_u32 s20, s20, 0x84180
	s_addc_u32 s21, s21, 0
	s_add_u32 s8, s8, 0x200
	s_addc_u32 s9, s9, 0
	s_mov_b64 s[48:49], 0x80000
	s_mov_b64 s[50:51], 0x80080
	s_mov_b64 s[52:53], 0xc0000
	s_mov_b64 s[54:55], 0xc0080
	s_mov_b64 s[56:57], 0xc6000
.LBB0_594:
	ds_read_b128 v[136:139], v116
	ds_read_b128 v[140:143], v116 offset:1024
	ds_read_b128 v[144:147], v116 offset:2048
	ds_read_b128 v[148:151], v116 offset:3072
	ds_read_b128 v[152:155], v117
	ds_read_b128 v[156:159], v117 offset:1024
	ds_read_b128 v[160:163], v117 offset:2048
	ds_read_b128 v[164:167], v117 offset:3072
	s_add_u32 s43, s20, 0xfff7c080
	s_addc_u32 s44, s21, -1
	s_cmp_eq_u32 s15, 28
	s_cselect_b32 s45, s17, s44
	s_cselect_b32 s44, s16, s43
	s_cselect_b32 s47, s4, s9
	s_cselect_b32 s46, s5, s8
	s_mov_b32 m0, s33
	v_lshl_add_u64 v[192:193], s[20:21], 0, v[200:201]
	ds_read_b128 v[168:171], v221
	ds_read_b128 v[172:175], v221 offset:1024
	ds_read_b128 v[176:179], v221 offset:2048
	ds_read_b128 v[180:183], v221 offset:3072
	ds_read_b128 v[184:187], v221 offset:4096
	ds_read_b128 v[188:191], v221 offset:5120
	ds_read_b128 v[202:205], v221 offset:6144
	ds_read_b128 v[206:209], v221 offset:7168
	global_load_lds_dwordx4 v[192:193], off
	v_lshl_add_u64 v[192:193], v[192:193], 0, s[96:97]
	s_mov_b32 m0, s34
	s_nop 0
	global_load_lds_dwordx4 v[192:193], off
	s_waitcnt vmcnt(8)
	s_waitcnt lgkmcnt(0)
	s_barrier
; #define PG8_MMA(ai, bj, At, Bt) do { __builtin_amdgcn_s_setprio(1); _Pragma("unroll") for (int m = 0; m < 4; ++m) _Pragma("unroll") for (int n = 0; n < 2; ++n) _Pragma("unroll") for (int k = 0; k < 2; ++k) \
;         acc[ai][bj][m][n] = __builtin_amdgcn_mfma_f32_16x16x32_bf16(Bt[n][k], At[m][k], acc[ai][bj][m][n], 0, 0, 0); __builtin_amdgcn_s_setprio(0); } while (0)
; #define PG8_WAIT_V(n) asm volatile("s_waitcnt vmcnt(" #n ")" ::: "memory")
; #define PG8_TRIP_HEAD(T) const int t = (T); const bool last = (t == nt - 2); \
;             const char* a1 = cA + (size_t)(t + 1) * kstep; \
;             const char* a2 = last ? nA : cA + (size_t)(t + 2) * kstep; const char* b2 = last ? nB : cB + (size_t)(t + 2) * kstep; \
;             const char* a3 = a2 + kstep; const char* b3 = b2 + kstep; \
;             if (last && has_next) S.a_ready(nxt);
; template <class Epi, class Sched, bool ALIGN_EPI = false, bool SP2 = false>
; __device__ __forceinline__ void gemm_phase(PG8_LAS unsigned char* lds, const Gemm g, const Sched& S, const Epi& E) {
;     ...
;         if constexpr (SP2) {
;             { PG8_TRIP_HEAD(0) PG8_TRIP_SP2(asm volatile("s_waitcnt vmcnt(%0)" :: "n"(8 + Epi::NST) : "memory"), PG8_MMAZ) }
;             for (int tt = 2; tt < nt; tt += 2) { PG8_TRIP_HEAD(tt) PG8_TRIP_SP2(PG8_WAIT_V(8), PG8_MMA) }
	s_waitcnt lgkmcnt(0)
	v_mfma_f32_16x16x32_bf16 v[130:133], v[136:139], v[168:171], v[130:133]
	v_mfma_f32_16x16x32_bf16 v[130:133], v[140:143], v[172:175], v[130:133]
	v_mfma_f32_16x16x32_bf16 v[126:129], v[144:147], v[168:171], v[126:129]
	v_mfma_f32_16x16x32_bf16 v[126:129], v[148:151], v[172:175], v[126:129]
	v_mfma_f32_16x16x32_bf16 v[112:115], v[136:139], v[176:179], v[112:115]
	v_mfma_f32_16x16x32_bf16 v[112:115], v[140:143], v[180:183], v[112:115]
	v_mfma_f32_16x16x32_bf16 v[108:111], v[144:147], v[176:179], v[108:111]
	v_mfma_f32_16x16x32_bf16 v[108:111], v[148:151], v[180:183], v[108:111]
	v_mfma_f32_16x16x32_bf16 v[96:99], v[136:139], v[184:187], v[96:99]
	v_mfma_f32_16x16x32_bf16 v[96:99], v[140:143], v[188:191], v[96:99]
	v_mfma_f32_16x16x32_bf16 v[92:95], v[144:147], v[184:187], v[92:95]
	v_mfma_f32_16x16x32_bf16 v[92:95], v[148:151], v[188:191], v[92:95]
	v_mfma_f32_16x16x32_bf16 v[80:83], v[136:139], v[202:205], v[80:83]
	v_mfma_f32_16x16x32_bf16 v[80:83], v[140:143], v[206:209], v[80:83]
	v_mfma_f32_16x16x32_bf16 v[76:79], v[144:147], v[202:205], v[76:79]
	v_mfma_f32_16x16x32_bf16 v[76:79], v[148:151], v[206:209], v[76:79]
	v_mfma_f32_16x16x32_bf16 v[122:125], v[152:155], v[168:171], v[122:125]
	v_mfma_f32_16x16x32_bf16 v[122:125], v[156:159], v[172:175], v[122:125]
	v_mfma_f32_16x16x32_bf16 v[118:121], v[160:163], v[168:171], v[118:121]
	v_mfma_f32_16x16x32_bf16 v[118:121], v[164:167], v[172:175], v[118:121]
	v_mfma_f32_16x16x32_bf16 v[104:107], v[152:155], v[176:179], v[104:107]
	v_mfma_f32_16x16x32_bf16 v[104:107], v[156:159], v[180:183], v[104:107]
	v_mfma_f32_16x16x32_bf16 v[100:103], v[160:163], v[176:179], v[100:103]
	v_mfma_f32_16x16x32_bf16 v[100:103], v[164:167], v[180:183], v[100:103]
	v_mfma_f32_16x16x32_bf16 v[88:91], v[152:155], v[184:187], v[88:91]
	v_mfma_f32_16x16x32_bf16 v[88:91], v[156:159], v[188:191], v[88:91]
	v_mfma_f32_16x16x32_bf16 v[84:87], v[160:163], v[184:187], v[84:87]
	v_mfma_f32_16x16x32_bf16 v[84:87], v[164:167], v[188:191], v[84:87]
	v_mfma_f32_16x16x32_bf16 v[72:75], v[152:155], v[202:205], v[72:75]
	v_mfma_f32_16x16x32_bf16 v[72:75], v[156:159], v[206:209], v[72:75]
	v_mfma_f32_16x16x32_bf16 v[68:71], v[160:163], v[202:205], v[68:71]
	v_mfma_f32_16x16x32_bf16 v[68:71], v[164:167], v[206:209], v[68:71]
	s_barrier
	s_mov_b32 m0, s35
	v_lshl_add_u64 v[192:193], s[46:47], 0, v[194:195]
	ds_read_b128 v[168:171], v221 offset:16384
	ds_read_b128 v[172:175], v221 offset:17408
	ds_read_b128 v[176:179], v221 offset:18432
	ds_read_b128 v[180:183], v221 offset:19456
	ds_read_b128 v[184:187], v221 offset:20480
	ds_read_b128 v[188:191], v221 offset:21504
	ds_read_b128 v[202:205], v221 offset:22528
	ds_read_b128 v[206:209], v221 offset:23552
	global_load_lds_dwordx4 v[192:193], off
	v_lshl_add_u64 v[214:215], v[192:193], 0, s[90:91]
	s_mov_b32 m0, s36
	s_nop 0
	global_load_lds_dwordx4 v[214:215], off
	v_lshl_add_u64 v[214:215], v[192:193], 0, s[48:49]
	s_mov_b32 m0, s37
	s_nop 0
	global_load_lds_dwordx4 v[214:215], off
	v_lshl_add_u64 v[214:215], v[192:193], 0, s[52:53]
	s_mov_b32 m0, s38
	s_nop 0
	global_load_lds_dwordx4 v[214:215], off
	v_lshl_add_u64 v[214:215], s[44:45], 0, v[196:197]
	s_mov_b32 m0, s23
	v_lshl_add_u64 v[216:217], v[214:215], 0, s[96:97]
	global_load_lds_dwordx4 v[214:215], off
	s_mov_b32 m0, s24
	s_nop 0
	global_load_lds_dwordx4 v[216:217], off
	s_waitcnt vmcnt(8)
	s_waitcnt lgkmcnt(0)
	s_barrier
	s_waitcnt lgkmcnt(0)
	v_mfma_f32_16x16x32_bf16 v[64:67], v[136:139], v[168:171], v[64:67]
	v_mfma_f32_16x16x32_bf16 v[64:67], v[140:143], v[172:175], v[64:67]
	v_mfma_f32_16x16x32_bf16 v[60:63], v[144:147], v[168:171], v[60:63]
	v_mfma_f32_16x16x32_bf16 v[60:63], v[148:151], v[172:175], v[60:63]
	v_mfma_f32_16x16x32_bf16 v[48:51], v[136:139], v[176:179], v[48:51]
	v_mfma_f32_16x16x32_bf16 v[48:51], v[140:143], v[180:183], v[48:51]
	v_mfma_f32_16x16x32_bf16 v[44:47], v[144:147], v[176:179], v[44:47]
	v_mfma_f32_16x16x32_bf16 v[44:47], v[148:151], v[180:183], v[44:47]
	v_mfma_f32_16x16x32_bf16 v[32:35], v[136:139], v[184:187], v[32:35]
	v_mfma_f32_16x16x32_bf16 v[32:35], v[140:143], v[188:191], v[32:35]
	v_mfma_f32_16x16x32_bf16 v[28:31], v[144:147], v[184:187], v[28:31]
	v_mfma_f32_16x16x32_bf16 v[28:31], v[148:151], v[188:191], v[28:31]
	v_mfma_f32_16x16x32_bf16 v[16:19], v[136:139], v[202:205], v[16:19]
	v_mfma_f32_16x16x32_bf16 v[16:19], v[140:143], v[206:209], v[16:19]
	v_mfma_f32_16x16x32_bf16 v[12:15], v[144:147], v[202:205], v[12:15]
	v_mfma_f32_16x16x32_bf16 v[12:15], v[148:151], v[206:209], v[12:15]
	v_mfma_f32_16x16x32_bf16 v[56:59], v[152:155], v[168:171], v[56:59]
	v_mfma_f32_16x16x32_bf16 v[56:59], v[156:159], v[172:175], v[56:59]
	v_mfma_f32_16x16x32_bf16 v[52:55], v[160:163], v[168:171], v[52:55]
	v_mfma_f32_16x16x32_bf16 v[52:55], v[164:167], v[172:175], v[52:55]
	v_mfma_f32_16x16x32_bf16 v[40:43], v[152:155], v[176:179], v[40:43]
	v_mfma_f32_16x16x32_bf16 v[40:43], v[156:159], v[180:183], v[40:43]
	v_mfma_f32_16x16x32_bf16 v[36:39], v[160:163], v[176:179], v[36:39]
	v_mfma_f32_16x16x32_bf16 v[36:39], v[164:167], v[180:183], v[36:39]
	v_mfma_f32_16x16x32_bf16 v[24:27], v[152:155], v[184:187], v[24:27]
	v_mfma_f32_16x16x32_bf16 v[24:27], v[156:159], v[188:191], v[24:27]
	v_mfma_f32_16x16x32_bf16 v[20:23], v[160:163], v[184:187], v[20:23]
	v_mfma_f32_16x16x32_bf16 v[20:23], v[164:167], v[188:191], v[20:23]
	v_mfma_f32_16x16x32_bf16 v[8:11], v[152:155], v[202:205], v[8:11]
	v_mfma_f32_16x16x32_bf16 v[8:11], v[156:159], v[206:209], v[8:11]
	v_mfma_f32_16x16x32_bf16 v[4:7], v[160:163], v[202:205], v[4:7]
	v_mfma_f32_16x16x32_bf16 v[4:7], v[164:167], v[206:209], v[4:7]
	s_barrier
; #define PG8_MMA(ai, bj, At, Bt) do { __builtin_amdgcn_s_setprio(1); _Pragma("unroll") for (int m = 0; m < 4; ++m) _Pragma("unroll") for (int n = 0; n < 2; ++n) _Pragma("unroll") for (int k = 0; k < 2; ++k) \
;         acc[ai][bj][m][n] = __builtin_amdgcn_mfma_f32_16x16x32_bf16(Bt[n][k], At[m][k], acc[ai][bj][m][n], 0, 0, 0); __builtin_amdgcn_s_setprio(0); } while (0)
; #define PG8_WAIT_V(n) asm volatile("s_waitcnt vmcnt(" #n ")" ::: "memory")
; #define PG8_BAR __builtin_amdgcn_s_barrier()
; #define PG8_TRIP_HEAD(T) const int t = (T); const bool last = (t == nt - 2); \
;             const char* a1 = cA + (size_t)(t + 1) * kstep; \
;             const char* a2 = last ? nA : cA + (size_t)(t + 2) * kstep; const char* b2 = last ? nB : cB + (size_t)(t + 2) * kstep; \
;             const char* a3 = a2 + kstep; const char* b3 = b2 + kstep; \
;             if (last && has_next) S.a_ready(nxt);
; template <class Epi, class Sched, bool ALIGN_EPI = false, bool SP2 = false>
; __device__ __forceinline__ void gemm_phase(PG8_LAS unsigned char* lds, const Gemm g, const Sched& S, const Epi& E) {
;     ...
;         if constexpr (SP2) {
;             { PG8_TRIP_HEAD(0) PG8_TRIP_SP2(asm volatile("s_waitcnt vmcnt(%0)" :: "n"(8 + Epi::NST) : "memory"), PG8_MMAZ) }
;             for (int tt = 2; tt < nt; tt += 2) { PG8_TRIP_HEAD(tt) PG8_TRIP_SP2(PG8_WAIT_V(8), PG8_MMA) }
;     ...
;         if constexpr (ALIGN_EPI) { if (wr == 0) PG8_BAR; }
	ds_read_b128 v[136:139], v134
	ds_read_b128 v[140:143], v134 offset:1024
	ds_read_b128 v[144:147], v134 offset:2048
	ds_read_b128 v[148:151], v134 offset:3072
	ds_read_b128 v[152:155], v135
	ds_read_b128 v[156:159], v135 offset:1024
	ds_read_b128 v[160:163], v135 offset:2048
	ds_read_b128 v[164:167], v135 offset:3072
	s_mov_b32 m0, s25
	v_lshl_add_u64 v[216:217], v[214:215], 0, s[82:83]
	ds_read_b128 v[168:171], v221 offset:32768
	ds_read_b128 v[172:175], v221 offset:33792
	ds_read_b128 v[176:179], v221 offset:34816
	ds_read_b128 v[180:183], v221 offset:35840
	ds_read_b128 v[184:187], v221 offset:36864
	ds_read_b128 v[188:191], v221 offset:37888
	ds_read_b128 v[202:205], v221 offset:38912
	ds_read_b128 v[206:209], v221 offset:39936
	global_load_lds_dwordx4 v[216:217], off
	v_lshl_add_u64 v[216:217], v[214:215], 0, s[56:57]
	s_mov_b32 m0, s26
	s_nop 0
	global_load_lds_dwordx4 v[216:217], off
	s_waitcnt vmcnt(8)
	s_waitcnt lgkmcnt(0)
	s_barrier
	s_waitcnt lgkmcnt(0)
	v_mfma_f32_16x16x32_bf16 v[130:133], v[136:139], v[168:171], v[130:133]
	v_mfma_f32_16x16x32_bf16 v[130:133], v[140:143], v[172:175], v[130:133]
	v_mfma_f32_16x16x32_bf16 v[126:129], v[144:147], v[168:171], v[126:129]
	v_mfma_f32_16x16x32_bf16 v[126:129], v[148:151], v[172:175], v[126:129]
	v_mfma_f32_16x16x32_bf16 v[112:115], v[136:139], v[176:179], v[112:115]
	v_mfma_f32_16x16x32_bf16 v[112:115], v[140:143], v[180:183], v[112:115]
	v_mfma_f32_16x16x32_bf16 v[108:111], v[144:147], v[176:179], v[108:111]
	v_mfma_f32_16x16x32_bf16 v[108:111], v[148:151], v[180:183], v[108:111]
	v_mfma_f32_16x16x32_bf16 v[96:99], v[136:139], v[184:187], v[96:99]
	v_mfma_f32_16x16x32_bf16 v[96:99], v[140:143], v[188:191], v[96:99]
	v_mfma_f32_16x16x32_bf16 v[92:95], v[144:147], v[184:187], v[92:95]
	v_mfma_f32_16x16x32_bf16 v[92:95], v[148:151], v[188:191], v[92:95]
	v_mfma_f32_16x16x32_bf16 v[80:83], v[136:139], v[202:205], v[80:83]
	v_mfma_f32_16x16x32_bf16 v[80:83], v[140:143], v[206:209], v[80:83]
	v_mfma_f32_16x16x32_bf16 v[76:79], v[144:147], v[202:205], v[76:79]
	v_mfma_f32_16x16x32_bf16 v[76:79], v[148:151], v[206:209], v[76:79]
	v_mfma_f32_16x16x32_bf16 v[122:125], v[152:155], v[168:171], v[122:125]
	v_mfma_f32_16x16x32_bf16 v[122:125], v[156:159], v[172:175], v[122:125]
	v_mfma_f32_16x16x32_bf16 v[118:121], v[160:163], v[168:171], v[118:121]
	v_mfma_f32_16x16x32_bf16 v[118:121], v[164:167], v[172:175], v[118:121]
	v_mfma_f32_16x16x32_bf16 v[104:107], v[152:155], v[176:179], v[104:107]
	v_mfma_f32_16x16x32_bf16 v[104:107], v[156:159], v[180:183], v[104:107]
	v_mfma_f32_16x16x32_bf16 v[100:103], v[160:163], v[176:179], v[100:103]
	v_mfma_f32_16x16x32_bf16 v[100:103], v[164:167], v[180:183], v[100:103]
	v_mfma_f32_16x16x32_bf16 v[88:91], v[152:155], v[184:187], v[88:91]
	v_mfma_f32_16x16x32_bf16 v[88:91], v[156:159], v[188:191], v[88:91]
	v_mfma_f32_16x16x32_bf16 v[84:87], v[160:163], v[184:187], v[84:87]
	v_mfma_f32_16x16x32_bf16 v[84:87], v[164:167], v[188:191], v[84:87]
	v_mfma_f32_16x16x32_bf16 v[72:75], v[152:155], v[202:205], v[72:75]
	v_mfma_f32_16x16x32_bf16 v[72:75], v[156:159], v[206:209], v[72:75]
	v_mfma_f32_16x16x32_bf16 v[68:71], v[160:163], v[202:205], v[68:71]
	v_mfma_f32_16x16x32_bf16 v[68:71], v[164:167], v[206:209], v[68:71]
	s_barrier
	s_mov_b32 m0, s39
	v_lshl_add_u64 v[216:217], v[192:193], 0, s[78:79]
	ds_read_b128 v[168:171], v221 offset:49152
	ds_read_b128 v[172:175], v221 offset:50176
	ds_read_b128 v[176:179], v221 offset:51200
	ds_read_b128 v[180:183], v221 offset:52224
	ds_read_b128 v[184:187], v221 offset:53248
	ds_read_b128 v[188:191], v221 offset:54272
	ds_read_b128 v[202:205], v221 offset:55296
	ds_read_b128 v[206:209], v221 offset:56320
	global_load_lds_dwordx4 v[216:217], off
	v_lshl_add_u64 v[216:217], v[192:193], 0, s[84:85]
	s_mov_b32 m0, s40
	s_nop 0
	global_load_lds_dwordx4 v[216:217], off
	v_lshl_add_u64 v[216:217], v[192:193], 0, s[50:51]
	s_mov_b32 m0, s41
	v_lshl_add_u64 v[192:193], v[192:193], 0, s[54:55]
	global_load_lds_dwordx4 v[216:217], off
	s_mov_b32 m0, s42
	s_nop 0
	global_load_lds_dwordx4 v[192:193], off
	v_lshl_add_u64 v[192:193], v[214:215], 0, s[78:79]
	s_mov_b32 m0, s27
	s_nop 0
	global_load_lds_dwordx4 v[192:193], off
	v_lshl_add_u64 v[192:193], v[214:215], 0, s[92:93]
	s_mov_b32 m0, s28
	s_nop 0
	global_load_lds_dwordx4 v[192:193], off
	s_waitcnt vmcnt(8)
	s_waitcnt lgkmcnt(0)
	s_barrier
	s_waitcnt lgkmcnt(0)
	v_mfma_f32_16x16x32_bf16 v[64:67], v[136:139], v[168:171], v[64:67]
	v_mfma_f32_16x16x32_bf16 v[64:67], v[140:143], v[172:175], v[64:67]
	v_mfma_f32_16x16x32_bf16 v[60:63], v[144:147], v[168:171], v[60:63]
	v_mfma_f32_16x16x32_bf16 v[60:63], v[148:151], v[172:175], v[60:63]
	v_mfma_f32_16x16x32_bf16 v[48:51], v[136:139], v[176:179], v[48:51]
	v_mfma_f32_16x16x32_bf16 v[48:51], v[140:143], v[180:183], v[48:51]
	v_mfma_f32_16x16x32_bf16 v[44:47], v[144:147], v[176:179], v[44:47]
	v_mfma_f32_16x16x32_bf16 v[44:47], v[148:151], v[180:183], v[44:47]
	v_mfma_f32_16x16x32_bf16 v[32:35], v[136:139], v[184:187], v[32:35]
	v_mfma_f32_16x16x32_bf16 v[32:35], v[140:143], v[188:191], v[32:35]
	v_mfma_f32_16x16x32_bf16 v[28:31], v[144:147], v[184:187], v[28:31]
	v_mfma_f32_16x16x32_bf16 v[28:31], v[148:151], v[188:191], v[28:31]
	v_mfma_f32_16x16x32_bf16 v[16:19], v[136:139], v[202:205], v[16:19]
	v_mfma_f32_16x16x32_bf16 v[16:19], v[140:143], v[206:209], v[16:19]
	v_mfma_f32_16x16x32_bf16 v[12:15], v[144:147], v[202:205], v[12:15]
	v_mfma_f32_16x16x32_bf16 v[12:15], v[148:151], v[206:209], v[12:15]
	v_mfma_f32_16x16x32_bf16 v[56:59], v[152:155], v[168:171], v[56:59]
	v_mfma_f32_16x16x32_bf16 v[56:59], v[156:159], v[172:175], v[56:59]
	v_mfma_f32_16x16x32_bf16 v[52:55], v[160:163], v[168:171], v[52:55]
	v_mfma_f32_16x16x32_bf16 v[52:55], v[164:167], v[172:175], v[52:55]
	v_mfma_f32_16x16x32_bf16 v[40:43], v[152:155], v[176:179], v[40:43]
	v_mfma_f32_16x16x32_bf16 v[40:43], v[156:159], v[180:183], v[40:43]
	v_mfma_f32_16x16x32_bf16 v[36:39], v[160:163], v[176:179], v[36:39]
	v_mfma_f32_16x16x32_bf16 v[36:39], v[164:167], v[180:183], v[36:39]
	v_mfma_f32_16x16x32_bf16 v[24:27], v[152:155], v[184:187], v[24:27]
	v_mfma_f32_16x16x32_bf16 v[24:27], v[156:159], v[188:191], v[24:27]
	v_mfma_f32_16x16x32_bf16 v[20:23], v[160:163], v[184:187], v[20:23]
	v_mfma_f32_16x16x32_bf16 v[20:23], v[164:167], v[188:191], v[20:23]
	v_mfma_f32_16x16x32_bf16 v[8:11], v[152:155], v[202:205], v[8:11]
	v_mfma_f32_16x16x32_bf16 v[8:11], v[156:159], v[206:209], v[8:11]
	v_mfma_f32_16x16x32_bf16 v[4:7], v[160:163], v[202:205], v[4:7]
	v_mfma_f32_16x16x32_bf16 v[4:7], v[164:167], v[206:209], v[4:7]
	s_barrier
	s_add_i32 s15, s15, 2
	s_add_u32 s20, s20, 0x100
	s_addc_u32 s21, s21, 0
	s_add_u32 s8, s8, 0x100
	s_addc_u32 s9, s9, 0
	s_cmp_gt_u32 s15, 29
	s_cbranch_scc0 .LBB0_594
	s_and_b64 vcc, exec, s[12:13]
	s_cbranch_vccz .LBB0_597
	s_barrier

;     __device__ bool next(int i, Unit& u) const { const int rounds = nwg / G; if (i >= rounds) return false; return StaticOrder::next(rounds - 1 - i, u); }
;     __device__ bool next(int i, Unit& u) const { const int rounds = nwg / G; if (i >= 2 * rounds) return false; const bool ok = StaticOrder::next(i >= rounds ? i - rounds : i, u); u.z = (i >= rounds) ? 1 : 0; return ok; }
; #define PG8_TRIP_HEAD(T) const int t = (T); const bool last = (t == nt - 2); \
;             const char* a1 = cA + (size_t)(t + 1) * kstep; \
;             const char* a2 = last ? nA : cA + (size_t)(t + 2) * kstep; const char* b2 = last ? nB : cB + (size_t)(t + 2) * kstep; \
;             const char* a3 = a2 + kstep; const char* b3 = b2 + kstep; \
;             if (last && has_next) S.a_ready(nxt);
; template <class Epi, class Sched, bool ALIGN_EPI = false, bool SP2 = false>
; __device__ __forceinline__ void gemm_phase(PG8_LAS unsigned char* lds, const Gemm g, const Sched& S, const Epi& E) {
;     ...
;         const bool has_next = S.next(ui + 1, nxt);
;         const char* nA = has_next ? (const char*)S.opA(g, nxt) + (size_t)nxt.pm * tstepA : cA; const char* nB = has_next ? (const char*)S.opB(g, nxt) + (size_t)nxt.pn * tstepB : cB;
;     ...
;         if constexpr (SP2) {
;             { PG8_TRIP_HEAD(0) PG8_TRIP_SP2(asm volatile("s_waitcnt vmcnt(%0)" :: "n"(8 + Epi::NST) : "memory"), PG8_MMAZ) }
.LBB0_699:
	s_ashr_i32 s19, s18, 31
	s_lshl_b64 s[4:5], s[18:19], 20
	v_readlane_b32 s22, v254, 33
	v_readlane_b32 s23, v254, 34
	s_add_u32 s22, s22, s4
	s_addc_u32 s23, s23, s5
	s_add_i32 s33, 0, 0x10000
	s_add_i32 s41, 0, 0x14000
	v_add_u32_e32 v116, s33, v176
	v_add_u32_e32 v117, s41, v176
	ds_read_b128 v[4:7], v116
	ds_read_b128 v[8:11], v116 offset:1024
	ds_read_b128 v[12:15], v116 offset:2048
	ds_read_b128 v[16:19], v116 offset:3072
	ds_read_b128 v[20:23], v117
	ds_read_b128 v[24:27], v117 offset:1024
	ds_read_b128 v[28:31], v117 offset:2048
	ds_read_b128 v[32:35], v117 offset:3072
	s_and_b64 s[4:5], s[10:11], exec
	s_cselect_b32 s3, s23, s25
	s_cselect_b32 s4, s22, s24
	v_lshl_add_u64 v[208:209], s[26:27], 0, v[162:163]
	s_mov_b64 s[10:11], 0x84080
	s_add_i32 s5, s29, 0xc000
	v_lshl_add_u64 v[68:69], v[208:209], 0, s[10:11]
	s_mov_b32 m0, s5
	s_mov_b64 s[10:11], 0xc6080
	s_add_i32 s19, s29, 0xe000
	ds_read_b128 v[36:39], v178
	ds_read_b128 v[40:43], v178 offset:1024
	ds_read_b128 v[44:47], v178 offset:2048
	ds_read_b128 v[48:51], v178 offset:3072
	ds_read_b128 v[52:55], v178 offset:4096
	ds_read_b128 v[56:59], v178 offset:5120
	ds_read_b128 v[60:63], v178 offset:6144
	ds_read_b128 v[64:67], v178 offset:7168
	global_load_lds_dwordx4 v[68:69], off
	v_lshl_add_u64 v[68:69], v[208:209], 0, s[10:11]
	s_mov_b32 m0, s19
	s_nop 0
	global_load_lds_dwordx4 v[68:69], off
	s_waitcnt vmcnt(16)
	s_waitcnt lgkmcnt(0)
	s_barrier
	s_waitcnt lgkmcnt(0)
	v_mfma_f32_16x16x32_bf16 v[92:95], v[4:7], v[60:63], 0
	v_mfma_f32_16x16x32_bf16 v[68:71], v[4:7], v[36:39], 0
	v_mfma_f32_16x16x32_bf16 v[72:75], v[12:15], v[36:39], 0
	v_mfma_f32_16x16x32_bf16 v[76:79], v[4:7], v[44:47], 0
	v_mfma_f32_16x16x32_bf16 v[80:83], v[12:15], v[44:47], 0
	v_mfma_f32_16x16x32_bf16 v[84:87], v[4:7], v[52:55], 0
	v_mfma_f32_16x16x32_bf16 v[88:91], v[12:15], v[52:55], 0
	v_mfma_f32_16x16x32_bf16 v[100:103], v[8:11], v[64:67], v[92:95]
	v_mfma_f32_16x16x32_bf16 v[92:95], v[12:15], v[60:63], 0
	v_mfma_f32_16x16x32_bf16 v[68:71], v[8:11], v[40:43], v[68:71]
	v_mfma_f32_16x16x32_bf16 v[72:75], v[16:19], v[40:43], v[72:75]
	v_mfma_f32_16x16x32_bf16 v[76:79], v[8:11], v[48:51], v[76:79]
	v_mfma_f32_16x16x32_bf16 v[80:83], v[16:19], v[48:51], v[80:83]
	v_mfma_f32_16x16x32_bf16 v[84:87], v[8:11], v[56:59], v[84:87]
	v_mfma_f32_16x16x32_bf16 v[88:91], v[16:19], v[56:59], v[88:91]
	v_mfma_f32_16x16x32_bf16 v[104:107], v[16:19], v[64:67], v[92:95]
	v_mfma_f32_16x16x32_bf16 v[92:95], v[20:23], v[36:39], 0
	v_mfma_f32_16x16x32_bf16 v[36:39], v[28:31], v[36:39], 0
	v_mfma_f32_16x16x32_bf16 v[120:123], v[24:27], v[40:43], v[92:95]
	v_mfma_f32_16x16x32_bf16 v[36:39], v[32:35], v[40:43], v[36:39]
	v_mfma_f32_16x16x32_bf16 v[40:43], v[20:23], v[44:47], 0
	v_mfma_f32_16x16x32_bf16 v[44:47], v[28:31], v[44:47], 0
	v_mfma_f32_16x16x32_bf16 v[40:43], v[24:27], v[48:51], v[40:43]
	v_mfma_f32_16x16x32_bf16 v[44:47], v[32:35], v[48:51], v[44:47]
	v_mfma_f32_16x16x32_bf16 v[48:51], v[20:23], v[52:55], 0
	v_mfma_f32_16x16x32_bf16 v[52:55], v[28:31], v[52:55], 0
	v_mfma_f32_16x16x32_bf16 v[48:51], v[24:27], v[56:59], v[48:51]
	v_mfma_f32_16x16x32_bf16 v[52:55], v[32:35], v[56:59], v[52:55]
	v_mfma_f32_16x16x32_bf16 v[56:59], v[20:23], v[60:63], 0
	v_mfma_f32_16x16x32_bf16 v[60:63], v[28:31], v[60:63], 0
	v_mfma_f32_16x16x32_bf16 v[56:59], v[24:27], v[64:67], v[56:59]
	v_mfma_f32_16x16x32_bf16 v[60:63], v[32:35], v[64:67], v[60:63]
	s_barrier
	v_lshl_add_u64 v[250:251], s[24:25], 0, v[160:161]
	s_mov_b64 s[10:11], 0x100
	s_add_i32 s33, s33, s28
	v_lshl_add_u64 v[118:119], v[250:251], 0, s[10:11]
	s_mov_b32 m0, s33
	s_mov_b64 s[42:43], 0x40100
	s_add_i32 s40, s33, 0x2000
	ds_read_b128 v[64:67], v178 offset:16384
	ds_read_b128 v[92:95], v178 offset:17408
	ds_read_b128 v[96:99], v178 offset:18432
	ds_read_b128 v[108:111], v178 offset:19456
	ds_read_b128 v[112:115], v178 offset:20480
	ds_read_b128 v[124:127], v178 offset:21504
	ds_read_b128 v[128:131], v178 offset:22528
	ds_read_b128 v[132:135], v178 offset:23552
	global_load_lds_dwordx4 v[118:119], off
	v_lshl_add_u64 v[118:119], v[250:251], 0, s[42:43]
	s_mov_b32 m0, s40
	s_mov_b64 s[42:43], 0x80100
	s_add_i32 s41, s41, s28
	global_load_lds_dwordx4 v[118:119], off
	v_lshl_add_u64 v[118:119], v[250:251], 0, s[42:43]
	s_mov_b32 m0, s41
	s_mov_b64 s[42:43], 0xc0100
	global_load_lds_dwordx4 v[118:119], off
	v_lshl_add_u64 v[118:119], v[250:251], 0, s[42:43]
	s_add_i32 s42, s41, 0x2000
	s_mov_b32 m0, s42
	s_nop 0
	global_load_lds_dwordx4 v[118:119], off
	v_lshl_add_u64 v[118:119], v[208:209], 0, s[10:11]
	s_mov_b32 m0, s29
	s_mov_b64 s[10:11], 0x42100
	global_load_lds_dwordx4 v[118:119], off
	v_lshl_add_u64 v[118:119], v[208:209], 0, s[10:11]
	s_mov_b32 m0, s30
	s_nop 0
	global_load_lds_dwordx4 v[118:119], off
	s_waitcnt vmcnt(16)
	s_waitcnt lgkmcnt(0)
	s_barrier
; #define PG8_TRIP_HEAD(T) const int t = (T); const bool last = (t == nt - 2); \
;             const char* a1 = cA + (size_t)(t + 1) * kstep; \
;             const char* a2 = last ? nA : cA + (size_t)(t + 2) * kstep; const char* b2 = last ? nB : cB + (size_t)(t + 2) * kstep; \
;             const char* a3 = a2 + kstep; const char* b3 = b2 + kstep; \
;             if (last && has_next) S.a_ready(nxt);
; template <class Epi, class Sched, bool ALIGN_EPI = false, bool SP2 = false>
; __device__ __forceinline__ void gemm_phase(PG8_LAS unsigned char* lds, const Gemm g, const Sched& S, const Epi& E) {
;     ...
;         if constexpr (SP2) {
;             { PG8_TRIP_HEAD(0) PG8_TRIP_SP2(asm volatile("s_waitcnt vmcnt(%0)" :: "n"(8 + Epi::NST) : "memory"), PG8_MMAZ) }
	s_waitcnt lgkmcnt(0)
	v_mfma_f32_16x16x32_bf16 v[136:139], v[4:7], v[64:67], 0
	v_mfma_f32_16x16x32_bf16 v[144:147], v[8:11], v[92:95], v[136:139]
	v_mfma_f32_16x16x32_bf16 v[136:139], v[12:15], v[64:67], 0
	v_mfma_f32_16x16x32_bf16 v[148:151], v[16:19], v[92:95], v[136:139]
	v_mfma_f32_16x16x32_bf16 v[136:139], v[4:7], v[96:99], 0
	v_mfma_f32_16x16x32_bf16 v[152:155], v[8:11], v[108:111], v[136:139]
	v_mfma_f32_16x16x32_bf16 v[136:139], v[12:15], v[96:99], 0
	v_mfma_f32_16x16x32_bf16 v[156:159], v[16:19], v[108:111], v[136:139]
	v_mfma_f32_16x16x32_bf16 v[136:139], v[4:7], v[112:115], 0
	v_mfma_f32_16x16x32_bf16 v[4:7], v[4:7], v[128:131], 0
	v_mfma_f32_16x16x32_bf16 v[166:169], v[8:11], v[124:127], v[136:139]
	v_mfma_f32_16x16x32_bf16 v[4:7], v[8:11], v[132:135], v[4:7]
	v_mfma_f32_16x16x32_bf16 v[8:11], v[12:15], v[128:131], 0
	v_mfma_f32_16x16x32_bf16 v[136:139], v[12:15], v[112:115], 0
	v_mfma_f32_16x16x32_bf16 v[8:11], v[16:19], v[132:135], v[8:11]
	v_mfma_f32_16x16x32_bf16 v[170:173], v[16:19], v[124:127], v[136:139]
	v_mfma_f32_16x16x32_bf16 v[12:15], v[20:23], v[64:67], 0
	v_mfma_f32_16x16x32_bf16 v[180:183], v[24:27], v[92:95], v[12:15]
	v_mfma_f32_16x16x32_bf16 v[12:15], v[28:31], v[64:67], 0
	v_mfma_f32_16x16x32_bf16 v[184:187], v[32:35], v[92:95], v[12:15]
	v_mfma_f32_16x16x32_bf16 v[12:15], v[20:23], v[96:99], 0
	v_mfma_f32_16x16x32_bf16 v[188:191], v[24:27], v[108:111], v[12:15]
	v_mfma_f32_16x16x32_bf16 v[12:15], v[28:31], v[96:99], 0
	v_mfma_f32_16x16x32_bf16 v[192:195], v[32:35], v[108:111], v[12:15]
	v_mfma_f32_16x16x32_bf16 v[12:15], v[20:23], v[112:115], 0
	v_mfma_f32_16x16x32_bf16 v[196:199], v[24:27], v[124:127], v[12:15]
	v_mfma_f32_16x16x32_bf16 v[12:15], v[28:31], v[112:115], 0
	v_mfma_f32_16x16x32_bf16 v[200:203], v[32:35], v[124:127], v[12:15]
	v_mfma_f32_16x16x32_bf16 v[12:15], v[20:23], v[128:131], 0
	v_mfma_f32_16x16x32_bf16 v[204:207], v[24:27], v[132:135], v[12:15]
	v_mfma_f32_16x16x32_bf16 v[12:15], v[28:31], v[128:131], 0
	v_mfma_f32_16x16x32_bf16 v[132:135], v[32:35], v[132:135], v[12:15]
	s_barrier
	s_add_i32 s43, 0, 0x18000
	s_add_i32 s45, 0, 0x1c000
	v_add_u32_e32 v118, s43, v176
	v_add_u32_e32 v119, s45, v176
	s_nop 0
	ds_read_b128 v[12:15], v118
	ds_read_b128 v[16:19], v118 offset:1024
	ds_read_b128 v[20:23], v118 offset:2048
	ds_read_b128 v[24:27], v118 offset:3072
	ds_read_b128 v[214:217], v119
	ds_read_b128 v[218:221], v119 offset:1024
	ds_read_b128 v[222:225], v119 offset:2048
	ds_read_b128 v[226:229], v119 offset:3072
	s_mov_b64 s[10:11], 0x84100
	s_mov_b32 m0, s31
	v_lshl_add_u64 v[92:93], v[208:209], 0, s[10:11]
	s_mov_b64 s[10:11], 0xc6100
	ds_read_b128 v[28:31], v178 offset:32768
	ds_read_b128 v[32:35], v178 offset:33792
	ds_read_b128 v[64:67], v178 offset:34816
	ds_read_b128 v[230:233], v178 offset:35840
	ds_read_b128 v[234:237], v178 offset:36864
	ds_read_b128 v[238:241], v178 offset:37888
	ds_read_b128 v[242:245], v178 offset:38912
	ds_read_b128 v[246:249], v178 offset:39936
	global_load_lds_dwordx4 v[92:93], off
	v_lshl_add_u64 v[92:93], v[208:209], 0, s[10:11]
	s_mov_b32 m0, s34
	s_nop 0
	global_load_lds_dwordx4 v[92:93], off
	s_waitcnt vmcnt(8)
	s_waitcnt lgkmcnt(0)
	s_barrier
	s_waitcnt lgkmcnt(0)
	v_mfma_f32_16x16x32_bf16 v[68:71], v[12:15], v[28:31], v[68:71]
	v_mfma_f32_16x16x32_bf16 v[140:143], v[16:19], v[32:35], v[68:71]
	v_mfma_f32_16x16x32_bf16 v[68:71], v[20:23], v[28:31], v[72:75]
	v_mfma_f32_16x16x32_bf16 v[136:139], v[24:27], v[32:35], v[68:71]
	v_mfma_f32_16x16x32_bf16 v[68:71], v[12:15], v[64:67], v[76:79]
	v_mfma_f32_16x16x32_bf16 v[112:115], v[16:19], v[230:233], v[68:71]
	v_mfma_f32_16x16x32_bf16 v[68:71], v[20:23], v[64:67], v[80:83]
	v_mfma_f32_16x16x32_bf16 v[108:111], v[24:27], v[230:233], v[68:71]
	v_mfma_f32_16x16x32_bf16 v[68:71], v[12:15], v[234:237], v[84:87]
	v_mfma_f32_16x16x32_bf16 v[96:99], v[16:19], v[238:241], v[68:71]
	v_mfma_f32_16x16x32_bf16 v[68:71], v[20:23], v[234:237], v[88:91]
	v_mfma_f32_16x16x32_bf16 v[92:95], v[24:27], v[238:241], v[68:71]
	v_mfma_f32_16x16x32_bf16 v[68:71], v[12:15], v[242:245], v[100:103]
	v_mfma_f32_16x16x32_bf16 v[80:83], v[16:19], v[246:249], v[68:71]
	v_mfma_f32_16x16x32_bf16 v[68:71], v[20:23], v[242:245], v[104:107]
	v_mfma_f32_16x16x32_bf16 v[76:79], v[24:27], v[246:249], v[68:71]
	v_mfma_f32_16x16x32_bf16 v[68:71], v[214:217], v[28:31], v[120:123]
	v_mfma_f32_16x16x32_bf16 v[28:31], v[222:225], v[28:31], v[36:39]
	v_mfma_f32_16x16x32_bf16 v[124:127], v[226:229], v[32:35], v[28:31]
	v_mfma_f32_16x16x32_bf16 v[28:31], v[214:217], v[64:67], v[40:43]
	v_mfma_f32_16x16x32_bf16 v[104:107], v[218:221], v[230:233], v[28:31]
	v_mfma_f32_16x16x32_bf16 v[28:31], v[222:225], v[64:67], v[44:47]
	v_mfma_f32_16x16x32_bf16 v[100:103], v[226:229], v[230:233], v[28:31]
	v_mfma_f32_16x16x32_bf16 v[28:31], v[214:217], v[234:237], v[48:51]
	v_mfma_f32_16x16x32_bf16 v[88:91], v[218:221], v[238:241], v[28:31]
	v_mfma_f32_16x16x32_bf16 v[28:31], v[222:225], v[234:237], v[52:55]
	v_mfma_f32_16x16x32_bf16 v[84:87], v[226:229], v[238:241], v[28:31]
	v_mfma_f32_16x16x32_bf16 v[28:31], v[214:217], v[242:245], v[56:59]
	v_mfma_f32_16x16x32_bf16 v[72:75], v[218:221], v[246:249], v[28:31]
	v_mfma_f32_16x16x32_bf16 v[28:31], v[222:225], v[242:245], v[60:63]
	v_mfma_f32_16x16x32_bf16 v[128:131], v[218:221], v[32:35], v[68:71]
	v_mfma_f32_16x16x32_bf16 v[68:71], v[226:229], v[246:249], v[28:31]
	s_barrier
; #define PG8_MMA(ai, bj, At, Bt) do { __builtin_amdgcn_s_setprio(1); _Pragma("unroll") for (int m = 0; m < 4; ++m) _Pragma("unroll") for (int n = 0; n < 2; ++n) _Pragma("unroll") for (int k = 0; k < 2; ++k) \
;         acc[ai][bj][m][n] = __builtin_amdgcn_mfma_f32_16x16x32_bf16(Bt[n][k], At[m][k], acc[ai][bj][m][n], 0, 0, 0); __builtin_amdgcn_s_setprio(0); } while (0)
; #define PG8_WAIT_V(n) asm volatile("s_waitcnt vmcnt(" #n ")" ::: "memory")
; #define PG8_TRIP_HEAD(T) const int t = (T); const bool last = (t == nt - 2); \
;             const char* a1 = cA + (size_t)(t + 1) * kstep; \
;             const char* a2 = last ? nA : cA + (size_t)(t + 2) * kstep; const char* b2 = last ? nB : cB + (size_t)(t + 2) * kstep; \
;             const char* a3 = a2 + kstep; const char* b3 = b2 + kstep; \
;             if (last && has_next) S.a_ready(nxt);
; template <class Epi, class Sched, bool ALIGN_EPI = false, bool SP2 = false>
; __device__ __forceinline__ void gemm_phase(PG8_LAS unsigned char* lds, const Gemm g, const Sched& S, const Epi& E) {
;     ...
;         if constexpr (SP2) {
;             { PG8_TRIP_HEAD(0) PG8_TRIP_SP2(asm volatile("s_waitcnt vmcnt(%0)" :: "n"(8 + Epi::NST) : "memory"), PG8_MMAZ) }
;             for (int tt = 2; tt < nt; tt += 2) { PG8_TRIP_HEAD(tt) PG8_TRIP_SP2(PG8_WAIT_V(8), PG8_MMA) }
	s_mov_b64 s[10:11], 0x180
	s_add_i32 s43, s43, s28
	s_nop 1
	v_lshl_add_u64 v[28:29], v[250:251], 0, s[10:11]
	s_mov_b32 m0, s43
	s_mov_b64 s[46:47], 0x40180
	s_add_i32 s44, s43, 0x2000
	ds_read_b128 v[36:39], v178 offset:49152
	ds_read_b128 v[40:43], v178 offset:50176
	ds_read_b128 v[120:123], v178 offset:51200
	ds_read_b128 v[230:233], v178 offset:52224
	ds_read_b128 v[234:237], v178 offset:53248
	ds_read_b128 v[238:241], v178 offset:54272
	ds_read_b128 v[242:245], v178 offset:55296
	ds_read_b128 v[246:249], v178 offset:56320
	global_load_lds_dwordx4 v[28:29], off
	v_lshl_add_u64 v[28:29], v[250:251], 0, s[46:47]
	s_mov_b32 m0, s44
	s_mov_b64 s[46:47], 0x80180
	s_add_i32 s45, s45, s28
	global_load_lds_dwordx4 v[28:29], off
	v_lshl_add_u64 v[28:29], v[250:251], 0, s[46:47]
	s_mov_b32 m0, s45
	s_mov_b64 s[46:47], 0xc0180
	global_load_lds_dwordx4 v[28:29], off
	v_lshl_add_u64 v[28:29], v[250:251], 0, s[46:47]
	s_add_i32 s46, s45, 0x2000
	s_mov_b32 m0, s46
	s_nop 0
	global_load_lds_dwordx4 v[28:29], off
	v_lshl_add_u64 v[28:29], v[208:209], 0, s[10:11]
	s_mov_b32 m0, s36
	s_mov_b64 s[10:11], 0x42180
	global_load_lds_dwordx4 v[28:29], off
	v_lshl_add_u64 v[28:29], v[208:209], 0, s[10:11]
	s_mov_b32 m0, s37
	s_nop 0
	global_load_lds_dwordx4 v[28:29], off
	s_waitcnt vmcnt(8)
	s_waitcnt lgkmcnt(0)
	s_barrier
	s_waitcnt lgkmcnt(0)
	v_mfma_f32_16x16x32_bf16 v[28:31], v[12:15], v[36:39], v[144:147]
	v_mfma_f32_16x16x32_bf16 v[56:59], v[16:19], v[40:43], v[28:31]
	v_mfma_f32_16x16x32_bf16 v[28:31], v[20:23], v[36:39], v[148:151]
	v_mfma_f32_16x16x32_bf16 v[52:55], v[24:27], v[40:43], v[28:31]
	v_mfma_f32_16x16x32_bf16 v[28:31], v[12:15], v[120:123], v[152:155]
	v_mfma_f32_16x16x32_bf16 v[48:51], v[16:19], v[230:233], v[28:31]
	v_mfma_f32_16x16x32_bf16 v[28:31], v[20:23], v[120:123], v[156:159]
	v_mfma_f32_16x16x32_bf16 v[44:47], v[24:27], v[230:233], v[28:31]
	v_mfma_f32_16x16x32_bf16 v[28:31], v[12:15], v[234:237], v[166:169]
	v_mfma_f32_16x16x32_bf16 v[4:7], v[12:15], v[242:245], v[4:7]
	v_mfma_f32_16x16x32_bf16 v[32:35], v[16:19], v[238:241], v[28:31]
	v_mfma_f32_16x16x32_bf16 v[28:31], v[20:23], v[234:237], v[170:173]
	v_mfma_f32_16x16x32_bf16 v[16:19], v[16:19], v[246:249], v[4:7]
	v_mfma_f32_16x16x32_bf16 v[4:7], v[20:23], v[242:245], v[8:11]
	v_mfma_f32_16x16x32_bf16 v[28:31], v[24:27], v[238:241], v[28:31]
	v_mfma_f32_16x16x32_bf16 v[12:15], v[24:27], v[246:249], v[4:7]
	v_mfma_f32_16x16x32_bf16 v[4:7], v[214:217], v[36:39], v[180:183]
	v_mfma_f32_16x16x32_bf16 v[64:67], v[218:221], v[40:43], v[4:7]
	v_mfma_f32_16x16x32_bf16 v[4:7], v[222:225], v[36:39], v[184:187]
	v_mfma_f32_16x16x32_bf16 v[60:63], v[226:229], v[40:43], v[4:7]
	v_mfma_f32_16x16x32_bf16 v[4:7], v[214:217], v[120:123], v[188:191]
	v_mfma_f32_16x16x32_bf16 v[40:43], v[218:221], v[230:233], v[4:7]
	v_mfma_f32_16x16x32_bf16 v[4:7], v[222:225], v[120:123], v[192:195]
	v_mfma_f32_16x16x32_bf16 v[36:39], v[226:229], v[230:233], v[4:7]
	v_mfma_f32_16x16x32_bf16 v[4:7], v[214:217], v[234:237], v[196:199]
	v_mfma_f32_16x16x32_bf16 v[24:27], v[218:221], v[238:241], v[4:7]
	v_mfma_f32_16x16x32_bf16 v[4:7], v[222:225], v[234:237], v[200:203]
	v_mfma_f32_16x16x32_bf16 v[20:23], v[226:229], v[238:241], v[4:7]
	v_mfma_f32_16x16x32_bf16 v[4:7], v[214:217], v[242:245], v[204:207]
	v_mfma_f32_16x16x32_bf16 v[8:11], v[218:221], v[246:249], v[4:7]
	v_mfma_f32_16x16x32_bf16 v[4:7], v[222:225], v[242:245], v[132:135]
	v_mfma_f32_16x16x32_bf16 v[4:7], v[226:229], v[246:249], v[4:7]
	s_barrier
	s_add_u32 s10, s26, 0x84180
	s_addc_u32 s11, s27, 0
	s_add_u32 s24, s24, 0x200
	s_addc_u32 s25, s25, 0
	s_mov_b32 s26, 0
	s_mov_b64 s[52:53], 0x80000
	s_mov_b64 s[54:55], 0x80080
	s_mov_b64 s[56:57], 0xc0000
	s_mov_b64 s[60:61], 0xc0080
	s_mov_b64 s[62:63], 0xc6000
.LBB0_700:
	ds_read_b128 v[120:123], v116
	ds_read_b128 v[132:135], v116 offset:1024
	ds_read_b128 v[144:147], v116 offset:2048
	ds_read_b128 v[148:151], v116 offset:3072
	ds_read_b128 v[152:155], v117
	ds_read_b128 v[156:159], v117 offset:1024
	ds_read_b128 v[166:169], v117 offset:2048
	ds_read_b128 v[170:173], v117 offset:3072
	s_add_u32 s27, s10, 0xfff7c080
	s_addc_u32 s47, s11, -1
	s_cmp_eq_u32 s26, 28
	s_cselect_b32 s49, s21, s47
	s_cselect_b32 s48, s20, s27
	s_cselect_b32 s51, s3, s25
	s_cselect_b32 s50, s4, s24
	s_mov_b32 m0, s5
	v_lshl_add_u64 v[208:209], s[10:11], 0, v[164:165]
	ds_read_b128 v[180:183], v178
	ds_read_b128 v[184:187], v178 offset:1024
	ds_read_b128 v[188:191], v178 offset:2048
	ds_read_b128 v[192:195], v178 offset:3072
	ds_read_b128 v[196:199], v178 offset:4096
	ds_read_b128 v[200:203], v178 offset:5120
	ds_read_b128 v[204:207], v178 offset:6144
	ds_read_b128 v[214:217], v178 offset:7168
	global_load_lds_dwordx4 v[208:209], off
	v_lshl_add_u64 v[208:209], v[208:209], 0, s[96:97]
	s_mov_b32 m0, s19
	s_nop 0
	global_load_lds_dwordx4 v[208:209], off
	s_waitcnt vmcnt(8)
	s_waitcnt lgkmcnt(0)
	s_barrier
; #define PG8_MMA(ai, bj, At, Bt) do { __builtin_amdgcn_s_setprio(1); _Pragma("unroll") for (int m = 0; m < 4; ++m) _Pragma("unroll") for (int n = 0; n < 2; ++n) _Pragma("unroll") for (int k = 0; k < 2; ++k) \
;         acc[ai][bj][m][n] = __builtin_amdgcn_mfma_f32_16x16x32_bf16(Bt[n][k], At[m][k], acc[ai][bj][m][n], 0, 0, 0); __builtin_amdgcn_s_setprio(0); } while (0)
; #define PG8_WAIT_V(n) asm volatile("s_waitcnt vmcnt(" #n ")" ::: "memory")
; #define PG8_TRIP_HEAD(T) const int t = (T); const bool last = (t == nt - 2); \
;             const char* a1 = cA + (size_t)(t + 1) * kstep; \
;             const char* a2 = last ? nA : cA + (size_t)(t + 2) * kstep; const char* b2 = last ? nB : cB + (size_t)(t + 2) * kstep; \
;             const char* a3 = a2 + kstep; const char* b3 = b2 + kstep; \
;             if (last && has_next) S.a_ready(nxt);
; template <class Epi, class Sched, bool ALIGN_EPI = false, bool SP2 = false>
; __device__ __forceinline__ void gemm_phase(PG8_LAS unsigned char* lds, const Gemm g, const Sched& S, const Epi& E) {
;     ...
;         if constexpr (SP2) {
;             { PG8_TRIP_HEAD(0) PG8_TRIP_SP2(asm volatile("s_waitcnt vmcnt(%0)" :: "n"(8 + Epi::NST) : "memory"), PG8_MMAZ) }
;             for (int tt = 2; tt < nt; tt += 2) { PG8_TRIP_HEAD(tt) PG8_TRIP_SP2(PG8_WAIT_V(8), PG8_MMA) }
	s_waitcnt lgkmcnt(0)
	v_mfma_f32_16x16x32_bf16 v[140:143], v[120:123], v[180:183], v[140:143]
	v_mfma_f32_16x16x32_bf16 v[140:143], v[132:135], v[184:187], v[140:143]
	v_mfma_f32_16x16x32_bf16 v[136:139], v[144:147], v[180:183], v[136:139]
	v_mfma_f32_16x16x32_bf16 v[136:139], v[148:151], v[184:187], v[136:139]
	v_mfma_f32_16x16x32_bf16 v[112:115], v[120:123], v[188:191], v[112:115]
	v_mfma_f32_16x16x32_bf16 v[112:115], v[132:135], v[192:195], v[112:115]
	v_mfma_f32_16x16x32_bf16 v[108:111], v[144:147], v[188:191], v[108:111]
	v_mfma_f32_16x16x32_bf16 v[108:111], v[148:151], v[192:195], v[108:111]
	v_mfma_f32_16x16x32_bf16 v[96:99], v[120:123], v[196:199], v[96:99]
	v_mfma_f32_16x16x32_bf16 v[96:99], v[132:135], v[200:203], v[96:99]
	v_mfma_f32_16x16x32_bf16 v[92:95], v[144:147], v[196:199], v[92:95]
	v_mfma_f32_16x16x32_bf16 v[92:95], v[148:151], v[200:203], v[92:95]
	v_mfma_f32_16x16x32_bf16 v[80:83], v[120:123], v[204:207], v[80:83]
	v_mfma_f32_16x16x32_bf16 v[80:83], v[132:135], v[214:217], v[80:83]
	v_mfma_f32_16x16x32_bf16 v[76:79], v[144:147], v[204:207], v[76:79]
	v_mfma_f32_16x16x32_bf16 v[76:79], v[148:151], v[214:217], v[76:79]
	v_mfma_f32_16x16x32_bf16 v[128:131], v[152:155], v[180:183], v[128:131]
	v_mfma_f32_16x16x32_bf16 v[128:131], v[156:159], v[184:187], v[128:131]
	v_mfma_f32_16x16x32_bf16 v[124:127], v[166:169], v[180:183], v[124:127]
	v_mfma_f32_16x16x32_bf16 v[124:127], v[170:173], v[184:187], v[124:127]
	v_mfma_f32_16x16x32_bf16 v[104:107], v[152:155], v[188:191], v[104:107]
	v_mfma_f32_16x16x32_bf16 v[104:107], v[156:159], v[192:195], v[104:107]
	v_mfma_f32_16x16x32_bf16 v[100:103], v[166:169], v[188:191], v[100:103]
	v_mfma_f32_16x16x32_bf16 v[100:103], v[170:173], v[192:195], v[100:103]
	v_mfma_f32_16x16x32_bf16 v[88:91], v[152:155], v[196:199], v[88:91]
	v_mfma_f32_16x16x32_bf16 v[88:91], v[156:159], v[200:203], v[88:91]
	v_mfma_f32_16x16x32_bf16 v[84:87], v[166:169], v[196:199], v[84:87]
	v_mfma_f32_16x16x32_bf16 v[84:87], v[170:173], v[200:203], v[84:87]
	v_mfma_f32_16x16x32_bf16 v[72:75], v[152:155], v[204:207], v[72:75]
	v_mfma_f32_16x16x32_bf16 v[72:75], v[156:159], v[214:217], v[72:75]
	v_mfma_f32_16x16x32_bf16 v[68:71], v[166:169], v[204:207], v[68:71]
	v_mfma_f32_16x16x32_bf16 v[68:71], v[170:173], v[214:217], v[68:71]
	s_barrier
	s_mov_b32 m0, s33
	v_lshl_add_u64 v[208:209], s[50:51], 0, v[160:161]
	ds_read_b128 v[180:183], v178 offset:16384
	ds_read_b128 v[184:187], v178 offset:17408
	ds_read_b128 v[188:191], v178 offset:18432
	ds_read_b128 v[192:195], v178 offset:19456
	ds_read_b128 v[196:199], v178 offset:20480
	ds_read_b128 v[200:203], v178 offset:21504
	ds_read_b128 v[204:207], v178 offset:22528
	ds_read_b128 v[214:217], v178 offset:23552
	global_load_lds_dwordx4 v[208:209], off
	v_lshl_add_u64 v[218:219], v[208:209], 0, s[90:91]
	s_mov_b32 m0, s40
	s_nop 0
	global_load_lds_dwordx4 v[218:219], off
	v_lshl_add_u64 v[218:219], v[208:209], 0, s[52:53]
	s_mov_b32 m0, s41
	s_nop 0
	global_load_lds_dwordx4 v[218:219], off
	v_lshl_add_u64 v[218:219], v[208:209], 0, s[56:57]
	s_mov_b32 m0, s42
	s_nop 0
	global_load_lds_dwordx4 v[218:219], off
	v_lshl_add_u64 v[218:219], s[48:49], 0, v[162:163]
	s_mov_b32 m0, s29
	v_lshl_add_u64 v[220:221], v[218:219], 0, s[96:97]
	global_load_lds_dwordx4 v[218:219], off
	s_mov_b32 m0, s30
	s_nop 0
	global_load_lds_dwordx4 v[220:221], off
	s_waitcnt vmcnt(8)
	s_waitcnt lgkmcnt(0)
	s_barrier
	s_waitcnt lgkmcnt(0)
	v_mfma_f32_16x16x32_bf16 v[56:59], v[120:123], v[180:183], v[56:59]
	v_mfma_f32_16x16x32_bf16 v[56:59], v[132:135], v[184:187], v[56:59]
	v_mfma_f32_16x16x32_bf16 v[52:55], v[144:147], v[180:183], v[52:55]
	v_mfma_f32_16x16x32_bf16 v[52:55], v[148:151], v[184:187], v[52:55]
	v_mfma_f32_16x16x32_bf16 v[48:51], v[120:123], v[188:191], v[48:51]
	v_mfma_f32_16x16x32_bf16 v[48:51], v[132:135], v[192:195], v[48:51]
	v_mfma_f32_16x16x32_bf16 v[44:47], v[144:147], v[188:191], v[44:47]
	v_mfma_f32_16x16x32_bf16 v[44:47], v[148:151], v[192:195], v[44:47]
	v_mfma_f32_16x16x32_bf16 v[32:35], v[120:123], v[196:199], v[32:35]
	v_mfma_f32_16x16x32_bf16 v[32:35], v[132:135], v[200:203], v[32:35]
	v_mfma_f32_16x16x32_bf16 v[28:31], v[144:147], v[196:199], v[28:31]
	v_mfma_f32_16x16x32_bf16 v[28:31], v[148:151], v[200:203], v[28:31]
	v_mfma_f32_16x16x32_bf16 v[16:19], v[120:123], v[204:207], v[16:19]
	v_mfma_f32_16x16x32_bf16 v[16:19], v[132:135], v[214:217], v[16:19]
	v_mfma_f32_16x16x32_bf16 v[12:15], v[144:147], v[204:207], v[12:15]
	v_mfma_f32_16x16x32_bf16 v[12:15], v[148:151], v[214:217], v[12:15]
	v_mfma_f32_16x16x32_bf16 v[64:67], v[152:155], v[180:183], v[64:67]
	v_mfma_f32_16x16x32_bf16 v[64:67], v[156:159], v[184:187], v[64:67]
	v_mfma_f32_16x16x32_bf16 v[60:63], v[166:169], v[180:183], v[60:63]
	v_mfma_f32_16x16x32_bf16 v[60:63], v[170:173], v[184:187], v[60:63]
	v_mfma_f32_16x16x32_bf16 v[40:43], v[152:155], v[188:191], v[40:43]
	v_mfma_f32_16x16x32_bf16 v[40:43], v[156:159], v[192:195], v[40:43]
	v_mfma_f32_16x16x32_bf16 v[36:39], v[166:169], v[188:191], v[36:39]
	v_mfma_f32_16x16x32_bf16 v[36:39], v[170:173], v[192:195], v[36:39]
	v_mfma_f32_16x16x32_bf16 v[24:27], v[152:155], v[196:199], v[24:27]
	v_mfma_f32_16x16x32_bf16 v[24:27], v[156:159], v[200:203], v[24:27]
	v_mfma_f32_16x16x32_bf16 v[20:23], v[166:169], v[196:199], v[20:23]
	v_mfma_f32_16x16x32_bf16 v[20:23], v[170:173], v[200:203], v[20:23]
	v_mfma_f32_16x16x32_bf16 v[8:11], v[152:155], v[204:207], v[8:11]
	v_mfma_f32_16x16x32_bf16 v[8:11], v[156:159], v[214:217], v[8:11]
	v_mfma_f32_16x16x32_bf16 v[4:7], v[166:169], v[204:207], v[4:7]
	v_mfma_f32_16x16x32_bf16 v[4:7], v[170:173], v[214:217], v[4:7]
	s_barrier
; #define PG8_MMA(ai, bj, At, Bt) do { __builtin_amdgcn_s_setprio(1); _Pragma("unroll") for (int m = 0; m < 4; ++m) _Pragma("unroll") for (int n = 0; n < 2; ++n) _Pragma("unroll") for (int k = 0; k < 2; ++k) \
;         acc[ai][bj][m][n] = __builtin_amdgcn_mfma_f32_16x16x32_bf16(Bt[n][k], At[m][k], acc[ai][bj][m][n], 0, 0, 0); __builtin_amdgcn_s_setprio(0); } while (0)
; #define PG8_WAIT_V(n) asm volatile("s_waitcnt vmcnt(" #n ")" ::: "memory")
; #define PG8_BAR __builtin_amdgcn_s_barrier()
; #define PG8_TRIP_HEAD(T) const int t = (T); const bool last = (t == nt - 2); \
;             const char* a1 = cA + (size_t)(t + 1) * kstep; \
;             const char* a2 = last ? nA : cA + (size_t)(t + 2) * kstep; const char* b2 = last ? nB : cB + (size_t)(t + 2) * kstep; \
;             const char* a3 = a2 + kstep; const char* b3 = b2 + kstep; \
;             if (last && has_next) S.a_ready(nxt);
; template <class Epi, class Sched, bool ALIGN_EPI = false, bool SP2 = false>
; __device__ __forceinline__ void gemm_phase(PG8_LAS unsigned char* lds, const Gemm g, const Sched& S, const Epi& E) {
;     ...
;         if constexpr (SP2) {
;             { PG8_TRIP_HEAD(0) PG8_TRIP_SP2(asm volatile("s_waitcnt vmcnt(%0)" :: "n"(8 + Epi::NST) : "memory"), PG8_MMAZ) }
;             for (int tt = 2; tt < nt; tt += 2) { PG8_TRIP_HEAD(tt) PG8_TRIP_SP2(PG8_WAIT_V(8), PG8_MMA) }
;     ...
;         if constexpr (ALIGN_EPI) { if (wr == 0) PG8_BAR; }
	ds_read_b128 v[120:123], v118
	ds_read_b128 v[132:135], v118 offset:1024
	ds_read_b128 v[144:147], v118 offset:2048
	ds_read_b128 v[148:151], v118 offset:3072
	ds_read_b128 v[152:155], v119
	ds_read_b128 v[156:159], v119 offset:1024
	ds_read_b128 v[166:169], v119 offset:2048
	ds_read_b128 v[170:173], v119 offset:3072
	s_mov_b32 m0, s31
	v_lshl_add_u64 v[220:221], v[218:219], 0, s[82:83]
	ds_read_b128 v[180:183], v178 offset:32768
	ds_read_b128 v[184:187], v178 offset:33792
	ds_read_b128 v[188:191], v178 offset:34816
	ds_read_b128 v[192:195], v178 offset:35840
	ds_read_b128 v[196:199], v178 offset:36864
	ds_read_b128 v[200:203], v178 offset:37888
	ds_read_b128 v[204:207], v178 offset:38912
	ds_read_b128 v[214:217], v178 offset:39936
	global_load_lds_dwordx4 v[220:221], off
	v_lshl_add_u64 v[220:221], v[218:219], 0, s[62:63]
	s_mov_b32 m0, s34
	s_nop 0
	global_load_lds_dwordx4 v[220:221], off
	s_waitcnt vmcnt(8)
	s_waitcnt lgkmcnt(0)
	s_barrier
	s_waitcnt lgkmcnt(0)
	v_mfma_f32_16x16x32_bf16 v[140:143], v[120:123], v[180:183], v[140:143]
	v_mfma_f32_16x16x32_bf16 v[140:143], v[132:135], v[184:187], v[140:143]
	v_mfma_f32_16x16x32_bf16 v[136:139], v[144:147], v[180:183], v[136:139]
	v_mfma_f32_16x16x32_bf16 v[136:139], v[148:151], v[184:187], v[136:139]
	v_mfma_f32_16x16x32_bf16 v[112:115], v[120:123], v[188:191], v[112:115]
	v_mfma_f32_16x16x32_bf16 v[112:115], v[132:135], v[192:195], v[112:115]
	v_mfma_f32_16x16x32_bf16 v[108:111], v[144:147], v[188:191], v[108:111]
	v_mfma_f32_16x16x32_bf16 v[108:111], v[148:151], v[192:195], v[108:111]
	v_mfma_f32_16x16x32_bf16 v[96:99], v[120:123], v[196:199], v[96:99]
	v_mfma_f32_16x16x32_bf16 v[96:99], v[132:135], v[200:203], v[96:99]
	v_mfma_f32_16x16x32_bf16 v[92:95], v[144:147], v[196:199], v[92:95]
	v_mfma_f32_16x16x32_bf16 v[92:95], v[148:151], v[200:203], v[92:95]
	v_mfma_f32_16x16x32_bf16 v[80:83], v[120:123], v[204:207], v[80:83]
	v_mfma_f32_16x16x32_bf16 v[80:83], v[132:135], v[214:217], v[80:83]
	v_mfma_f32_16x16x32_bf16 v[76:79], v[144:147], v[204:207], v[76:79]
	v_mfma_f32_16x16x32_bf16 v[76:79], v[148:151], v[214:217], v[76:79]
	v_mfma_f32_16x16x32_bf16 v[128:131], v[152:155], v[180:183], v[128:131]
	v_mfma_f32_16x16x32_bf16 v[128:131], v[156:159], v[184:187], v[128:131]
	v_mfma_f32_16x16x32_bf16 v[124:127], v[166:169], v[180:183], v[124:127]
	v_mfma_f32_16x16x32_bf16 v[124:127], v[170:173], v[184:187], v[124:127]
	v_mfma_f32_16x16x32_bf16 v[104:107], v[152:155], v[188:191], v[104:107]
	v_mfma_f32_16x16x32_bf16 v[104:107], v[156:159], v[192:195], v[104:107]
	v_mfma_f32_16x16x32_bf16 v[100:103], v[166:169], v[188:191], v[100:103]
	v_mfma_f32_16x16x32_bf16 v[100:103], v[170:173], v[192:195], v[100:103]
	v_mfma_f32_16x16x32_bf16 v[88:91], v[152:155], v[196:199], v[88:91]
	v_mfma_f32_16x16x32_bf16 v[88:91], v[156:159], v[200:203], v[88:91]
	v_mfma_f32_16x16x32_bf16 v[84:87], v[166:169], v[196:199], v[84:87]
	v_mfma_f32_16x16x32_bf16 v[84:87], v[170:173], v[200:203], v[84:87]
	v_mfma_f32_16x16x32_bf16 v[72:75], v[152:155], v[204:207], v[72:75]
	v_mfma_f32_16x16x32_bf16 v[72:75], v[156:159], v[214:217], v[72:75]
	v_mfma_f32_16x16x32_bf16 v[68:71], v[166:169], v[204:207], v[68:71]
	v_mfma_f32_16x16x32_bf16 v[68:71], v[170:173], v[214:217], v[68:71]
	s_barrier
	s_mov_b32 m0, s43
	v_lshl_add_u64 v[220:221], v[208:209], 0, s[78:79]
	ds_read_b128 v[180:183], v178 offset:49152
	ds_read_b128 v[184:187], v178 offset:50176
	ds_read_b128 v[188:191], v178 offset:51200
	ds_read_b128 v[192:195], v178 offset:52224
	ds_read_b128 v[196:199], v178 offset:53248
	ds_read_b128 v[200:203], v178 offset:54272
	ds_read_b128 v[204:207], v178 offset:55296
	ds_read_b128 v[214:217], v178 offset:56320
	global_load_lds_dwordx4 v[220:221], off
	v_lshl_add_u64 v[220:221], v[208:209], 0, s[84:85]
	s_mov_b32 m0, s44
	s_nop 0
	global_load_lds_dwordx4 v[220:221], off
	v_lshl_add_u64 v[220:221], v[208:209], 0, s[54:55]
	s_mov_b32 m0, s45
	v_lshl_add_u64 v[208:209], v[208:209], 0, s[60:61]
	global_load_lds_dwordx4 v[220:221], off
	s_mov_b32 m0, s46
	s_nop 0
	global_load_lds_dwordx4 v[208:209], off
	v_lshl_add_u64 v[208:209], v[218:219], 0, s[78:79]
	s_mov_b32 m0, s36
	s_nop 0
	global_load_lds_dwordx4 v[208:209], off
	v_lshl_add_u64 v[208:209], v[218:219], 0, s[92:93]
	s_mov_b32 m0, s37
	s_nop 0
	global_load_lds_dwordx4 v[208:209], off
	s_waitcnt vmcnt(8)
	s_waitcnt lgkmcnt(0)
	s_barrier
	s_waitcnt lgkmcnt(0)
	v_mfma_f32_16x16x32_bf16 v[56:59], v[120:123], v[180:183], v[56:59]
	v_mfma_f32_16x16x32_bf16 v[56:59], v[132:135], v[184:187], v[56:59]
	v_mfma_f32_16x16x32_bf16 v[52:55], v[144:147], v[180:183], v[52:55]
	v_mfma_f32_16x16x32_bf16 v[52:55], v[148:151], v[184:187], v[52:55]
	v_mfma_f32_16x16x32_bf16 v[48:51], v[120:123], v[188:191], v[48:51]
	v_mfma_f32_16x16x32_bf16 v[48:51], v[132:135], v[192:195], v[48:51]
	v_mfma_f32_16x16x32_bf16 v[44:47], v[144:147], v[188:191], v[44:47]
	v_mfma_f32_16x16x32_bf16 v[44:47], v[148:151], v[192:195], v[44:47]
	v_mfma_f32_16x16x32_bf16 v[32:35], v[120:123], v[196:199], v[32:35]
	v_mfma_f32_16x16x32_bf16 v[32:35], v[132:135], v[200:203], v[32:35]
	v_mfma_f32_16x16x32_bf16 v[28:31], v[144:147], v[196:199], v[28:31]
	v_mfma_f32_16x16x32_bf16 v[28:31], v[148:151], v[200:203], v[28:31]
	v_mfma_f32_16x16x32_bf16 v[16:19], v[120:123], v[204:207], v[16:19]
	v_mfma_f32_16x16x32_bf16 v[16:19], v[132:135], v[214:217], v[16:19]
	v_mfma_f32_16x16x32_bf16 v[12:15], v[144:147], v[204:207], v[12:15]
	v_mfma_f32_16x16x32_bf16 v[12:15], v[148:151], v[214:217], v[12:15]
	v_mfma_f32_16x16x32_bf16 v[64:67], v[152:155], v[180:183], v[64:67]
	v_mfma_f32_16x16x32_bf16 v[64:67], v[156:159], v[184:187], v[64:67]
	v_mfma_f32_16x16x32_bf16 v[60:63], v[166:169], v[180:183], v[60:63]
	v_mfma_f32_16x16x32_bf16 v[60:63], v[170:173], v[184:187], v[60:63]
	v_mfma_f32_16x16x32_bf16 v[40:43], v[152:155], v[188:191], v[40:43]
	v_mfma_f32_16x16x32_bf16 v[40:43], v[156:159], v[192:195], v[40:43]
	v_mfma_f32_16x16x32_bf16 v[36:39], v[166:169], v[188:191], v[36:39]
	v_mfma_f32_16x16x32_bf16 v[36:39], v[170:173], v[192:195], v[36:39]
	v_mfma_f32_16x16x32_bf16 v[24:27], v[152:155], v[196:199], v[24:27]
	v_mfma_f32_16x16x32_bf16 v[24:27], v[156:159], v[200:203], v[24:27]
	v_mfma_f32_16x16x32_bf16 v[20:23], v[166:169], v[196:199], v[20:23]
	v_mfma_f32_16x16x32_bf16 v[20:23], v[170:173], v[200:203], v[20:23]
	v_mfma_f32_16x16x32_bf16 v[8:11], v[152:155], v[204:207], v[8:11]
	v_mfma_f32_16x16x32_bf16 v[8:11], v[156:159], v[214:217], v[8:11]
	v_mfma_f32_16x16x32_bf16 v[4:7], v[166:169], v[204:207], v[4:7]
	v_mfma_f32_16x16x32_bf16 v[4:7], v[170:173], v[214:217], v[4:7]
	s_barrier
	s_add_i32 s26, s26, 2
	s_add_u32 s10, s10, 0x100
	s_addc_u32 s11, s11, 0
	s_add_u32 s24, s24, 0x100
	s_addc_u32 s25, s25, 0
	s_cmp_gt_u32 s26, 29
	s_cbranch_scc0 .LBB0_700
	s_and_b64 vcc, exec, s[16:17]
	s_cbranch_vccz .LBB0_703
	s_barrier
